# k_qkv_temporal at 128 VGPRs and 40960 B LDS (four workgroups per CU): minimal-footprint K loop, epilogue LDS scratch areas re-based into unused QKh rows
# speedup vs baseline: 1.0154x; 1.0097x over previous
_Z14k_qkv_temporalPKDF16_S0_PKfPDF16_S3_S3_PfPi:
	s_load_dwordx4 s[36:39], s[0:1], 0x0
	s_load_dwordx2 s[40:41], s[0:1], 0x10
	s_load_dwordx4 s[8:11], s[0:1], 0x30
	s_and_b32 s3, s2, 7
	s_mul_i32 s3, s3, 0x71
	s_lshr_b32 s4, s2, 3
	s_add_u32 s3, s3, s4
	s_and_b32 s22, s3, 7
	s_lshr_b32 s16, s3, 3
	s_mul_i32 s16, s16, 14
	v_lshrrev_b32_e32 v1, 6, v0
	v_and_b32_e32 v92, 15, v0
	v_bfe_u32 v90, v0, 4, 2
	v_lshlrev_b32_e32 v95, 2, v90
	v_lshl_or_b32 v91, v1, 5, v95
	v_bfe_u32 v112, v0, 3, 3
	v_and_b32_e32 v113, 7, v0
	v_lshrrev_b32_e32 v114, 1, v112
	v_and_b32_e32 v115, 1, v1
	v_lshl_or_b32 v114, v115, 2, v114
	v_xor_b32_e32 v114, v113, v114
	v_lshlrev_b32_e32 v114, 4, v114
	v_lshl_or_b32 v115, v1, 3, v112
	s_mov_b32 s42, 0x12492493
	s_movk_i32 s43, 0x627
	s_movk_i32 s44, 0x628
	v_add_u32_e32 v116, 0, v115
	v_min_u32_e32 v116, 0x7d, v116
	v_mul_hi_u32 v112, v116, s42
	v_mul_u32_u24_e32 v113, 14, v112
	v_sub_u32_e32 v113, v116, v113
	v_add_u32_e32 v113, s16, v113
	v_min_u32_e32 v113, s43, v113
	v_mad_u32_u24 v113, v112, s44, v113
	v_lshl_or_b32 v100, v113, 10, v114
	v_add_u32_e32 v116, 32, v115
	v_min_u32_e32 v116, 0x7d, v116
	v_mul_hi_u32 v112, v116, s42
	v_mul_u32_u24_e32 v113, 14, v112
	v_sub_u32_e32 v113, v116, v113
	v_add_u32_e32 v113, s16, v113
	v_min_u32_e32 v113, s43, v113
	v_mad_u32_u24 v113, v112, s44, v113
	v_lshl_or_b32 v101, v113, 10, v114
	v_add_u32_e32 v116, 64, v115
	v_min_u32_e32 v116, 0x7d, v116
	v_mul_hi_u32 v112, v116, s42
	v_mul_u32_u24_e32 v113, 14, v112
	v_sub_u32_e32 v113, v116, v113
	v_add_u32_e32 v113, s16, v113
	v_min_u32_e32 v113, s43, v113
	v_mad_u32_u24 v113, v112, s44, v113
	v_lshl_or_b32 v102, v113, 10, v114
	v_add_u32_e32 v116, 96, v115
	v_min_u32_e32 v116, 0x7d, v116
	v_mul_hi_u32 v112, v116, s42
	v_mul_u32_u24_e32 v113, 14, v112
	v_sub_u32_e32 v113, v116, v113
	v_add_u32_e32 v113, s16, v113
	v_min_u32_e32 v113, s43, v113
	v_mad_u32_u24 v113, v112, s44, v113
	v_lshl_or_b32 v103, v113, 10, v114
	s_lshl_b32 s45, s22, 6
	v_add_u32_e32 v116, s45, v115
	v_lshl_or_b32 v120, v116, 10, v114
	v_lshlrev_b32_e32 v116, 10, v1
	s_nop 0
	v_readfirstlane_b32 s24, v116
	s_add_u32 s25, s24, 0x1000
	s_add_u32 s26, s24, 0x2000
	s_add_u32 s27, s24, 0x3000
	s_add_u32 s28, s24, 0x4000
	s_add_u32 s29, s24, 0x5000
	s_add_u32 s30, s24, 0x6000
	s_add_u32 s31, s24, 0x7000
	s_add_u32 s32, s24, 0x8000
	s_add_u32 s33, s24, 0x9000
	v_lshrrev_b32_e32 v116, 1, v92
	v_xor_b32_e32 v116, v90, v116
	v_lshlrev_b32_e32 v116, 4, v116
	v_lshl_or_b32 v121, v92, 7, v116
	v_xor_b32_e32 v122, 64, v121
	v_lshlrev_b32_e32 v116, 12, v1
	v_add_u32_e32 v93, v116, v121
	v_xor_b32_e32 v94, 64, v93
	v_lshl_add_u32 v117, s22, 6, v92
	v_lshlrev_b32_e32 v117, 2, v117
	v_add_u32_e32 v118, 0x1000, v117
	s_waitcnt lgkmcnt(0)
	s_add_u32 s46, s38, 0x8000
	s_addc_u32 s47, s39, 0
	s_add_u32 s48, s38, 0x80000
	s_addc_u32 s49, s39, 0
	s_add_u32 s50, s38, 0x88000
	s_addc_u32 s51, s39, 0
	s_add_u32 s52, s38, 0x100000
	s_addc_u32 s53, s39, 0
	s_add_u32 s54, s38, 0x108000
	s_addc_u32 s55, s39, 0
	global_load_dword v104, v117, s[40:41] offset:0
	global_load_dword v105, v117, s[40:41] offset:64
	global_load_dword v106, v117, s[40:41] offset:128
	global_load_dword v107, v117, s[40:41] offset:192
	global_load_dword v108, v117, s[40:41] offset:2048
	global_load_dword v109, v117, s[40:41] offset:2112
	global_load_dword v110, v117, s[40:41] offset:2176
	global_load_dword v111, v117, s[40:41] offset:2240
	global_load_dword v112, v118, s[40:41] offset:0
	global_load_dword v113, v118, s[40:41] offset:64
	global_load_dword v114, v118, s[40:41] offset:128
	global_load_dword v115, v118, s[40:41] offset:192
	s_mov_b32 m0, s24
	s_nop 0
	global_load_lds_dwordx4 v100, s[36:37]
	s_mov_b32 m0, s25
	s_nop 0
	global_load_lds_dwordx4 v101, s[36:37]
	s_mov_b32 m0, s26
	s_nop 0
	global_load_lds_dwordx4 v102, s[36:37]
	s_mov_b32 m0, s27
	s_nop 0
	global_load_lds_dwordx4 v103, s[36:37]
	s_add_u32 s36, s36, 0x80
	s_addc_u32 s37, s37, 0
	s_mov_b32 m0, s28
	s_nop 0
	global_load_lds_dwordx4 v120, s[38:39]
	s_mov_b32 m0, s29
	s_nop 0
	global_load_lds_dwordx4 v120, s[46:47]
	s_mov_b32 m0, s30
	s_nop 0
	global_load_lds_dwordx4 v120, s[48:49]
	s_mov_b32 m0, s31
	s_nop 0
	global_load_lds_dwordx4 v120, s[50:51]
	s_mov_b32 m0, s32
	s_nop 0
	global_load_lds_dwordx4 v120, s[52:53]
	s_mov_b32 m0, s33
	s_nop 0
	global_load_lds_dwordx4 v120, s[54:55]
	s_add_u32 s38, s38, 0x80
	s_addc_u32 s39, s39, 0
	s_add_u32 s46, s46, 0x80
	s_addc_u32 s47, s47, 0
	s_add_u32 s48, s48, 0x80
	s_addc_u32 s49, s49, 0
	s_add_u32 s50, s50, 0x80
	s_addc_u32 s51, s51, 0
	s_add_u32 s52, s52, 0x80
	s_addc_u32 s53, s53, 0
	s_add_u32 s54, s54, 0x80
	s_addc_u32 s55, s55, 0
	s_waitcnt vmcnt(10)
	v_mov_b32_e32 v124, v104
	v_mov_b32_e32 v125, v104
	v_mov_b32_e32 v126, v104
	v_mov_b32_e32 v127, v104
	v_mov_b32_e32 v62, v104
	v_mov_b32_e32 v63, v104
	v_mov_b32_e32 v64, v104
	v_mov_b32_e32 v65, v104
	v_mov_b32_e32 v86, v105
	v_mov_b32_e32 v87, v105
	v_mov_b32_e32 v88, v105
	v_mov_b32_e32 v89, v105
	v_mov_b32_e32 v58, v105
	v_mov_b32_e32 v59, v105
	v_mov_b32_e32 v60, v105
	v_mov_b32_e32 v61, v105
	v_mov_b32_e32 v96, v106
	v_mov_b32_e32 v97, v106
	v_mov_b32_e32 v98, v106
	v_mov_b32_e32 v99, v106
	v_mov_b32_e32 v54, v106
	v_mov_b32_e32 v55, v106
	v_mov_b32_e32 v56, v106
	v_mov_b32_e32 v57, v106
	v_mov_b32_e32 v82, v107
	v_mov_b32_e32 v83, v107
	v_mov_b32_e32 v84, v107
	v_mov_b32_e32 v85, v107
	v_mov_b32_e32 v50, v107
	v_mov_b32_e32 v51, v107
	v_mov_b32_e32 v52, v107
	v_mov_b32_e32 v53, v107
	v_mov_b32_e32 v78, v108
	v_mov_b32_e32 v79, v108
	v_mov_b32_e32 v80, v108
	v_mov_b32_e32 v81, v108
	v_mov_b32_e32 v46, v108
	v_mov_b32_e32 v47, v108
	v_mov_b32_e32 v48, v108
	v_mov_b32_e32 v49, v108
	v_mov_b32_e32 v74, v109
	v_mov_b32_e32 v75, v109
	v_mov_b32_e32 v76, v109
	v_mov_b32_e32 v77, v109
	v_mov_b32_e32 v42, v109
	v_mov_b32_e32 v43, v109
	v_mov_b32_e32 v44, v109
	v_mov_b32_e32 v45, v109
	v_mov_b32_e32 v70, v110
	v_mov_b32_e32 v71, v110
	v_mov_b32_e32 v72, v110
	v_mov_b32_e32 v73, v110
	v_mov_b32_e32 v38, v110
	v_mov_b32_e32 v39, v110
	v_mov_b32_e32 v40, v110
	v_mov_b32_e32 v41, v110
	v_mov_b32_e32 v66, v111
	v_mov_b32_e32 v67, v111
	v_mov_b32_e32 v68, v111
	v_mov_b32_e32 v69, v111
	v_mov_b32_e32 v34, v111
	v_mov_b32_e32 v35, v111
	v_mov_b32_e32 v36, v111
	v_mov_b32_e32 v37, v111
	v_mov_b32_e32 v18, v112
	v_mov_b32_e32 v19, v112
	v_mov_b32_e32 v20, v112
	v_mov_b32_e32 v21, v112
	v_mov_b32_e32 v2, v112
	v_mov_b32_e32 v3, v112
	v_mov_b32_e32 v4, v112
	v_mov_b32_e32 v5, v112
	v_mov_b32_e32 v26, v113
	v_mov_b32_e32 v27, v113
	v_mov_b32_e32 v28, v113
	v_mov_b32_e32 v29, v113
	v_mov_b32_e32 v10, v113
	v_mov_b32_e32 v11, v113
	v_mov_b32_e32 v12, v113
	v_mov_b32_e32 v13, v113
	v_mov_b32_e32 v22, v114
	v_mov_b32_e32 v23, v114
	v_mov_b32_e32 v24, v114
	v_mov_b32_e32 v25, v114
	v_mov_b32_e32 v6, v114
	v_mov_b32_e32 v7, v114
	v_mov_b32_e32 v8, v114
	v_mov_b32_e32 v9, v114
	v_mov_b32_e32 v30, v115
	v_mov_b32_e32 v31, v115
	v_mov_b32_e32 v32, v115
	v_mov_b32_e32 v33, v115
	v_mov_b32_e32 v14, v115
	v_mov_b32_e32 v15, v115
	v_mov_b32_e32 v16, v115
	v_mov_b32_e32 v17, v115
	s_waitcnt vmcnt(0)
	s_barrier
	ds_read_b128 v[104:107], v93 offset:0
	ds_read_b128 v[108:111], v93 offset:2048
	ds_read_b128 v[112:115], v121 offset:16384
	ds_read_b128 v[116:119], v121 offset:18432
	s_waitcnt lgkmcnt(1)
	v_mfma_f32_16x16x32_f16 v[124:127], v[104:107], v[112:115], v[124:127]
	v_mfma_f32_16x16x32_f16 v[62:65], v[108:111], v[112:115], v[62:65]
	ds_read_b128 v[112:115], v121 offset:20480
	s_waitcnt lgkmcnt(1)
	v_mfma_f32_16x16x32_f16 v[86:89], v[104:107], v[116:119], v[86:89]
	v_mfma_f32_16x16x32_f16 v[58:61], v[108:111], v[116:119], v[58:61]
	ds_read_b128 v[116:119], v121 offset:22528
	s_waitcnt lgkmcnt(1)
	v_mfma_f32_16x16x32_f16 v[96:99], v[104:107], v[112:115], v[96:99]
	v_mfma_f32_16x16x32_f16 v[54:57], v[108:111], v[112:115], v[54:57]
	ds_read_b128 v[112:115], v121 offset:24576
	s_waitcnt lgkmcnt(1)
	v_mfma_f32_16x16x32_f16 v[82:85], v[104:107], v[116:119], v[82:85]
	v_mfma_f32_16x16x32_f16 v[50:53], v[108:111], v[116:119], v[50:53]
	ds_read_b128 v[116:119], v121 offset:26624
	s_waitcnt lgkmcnt(1)
	v_mfma_f32_16x16x32_f16 v[78:81], v[104:107], v[112:115], v[78:81]
	v_mfma_f32_16x16x32_f16 v[46:49], v[108:111], v[112:115], v[46:49]
	ds_read_b128 v[112:115], v121 offset:28672
	s_waitcnt lgkmcnt(1)
	v_mfma_f32_16x16x32_f16 v[74:77], v[104:107], v[116:119], v[74:77]
	v_mfma_f32_16x16x32_f16 v[42:45], v[108:111], v[116:119], v[42:45]
	ds_read_b128 v[116:119], v121 offset:30720
	s_waitcnt lgkmcnt(1)
	v_mfma_f32_16x16x32_f16 v[70:73], v[104:107], v[112:115], v[70:73]
	v_mfma_f32_16x16x32_f16 v[38:41], v[108:111], v[112:115], v[38:41]
	ds_read_b128 v[112:115], v121 offset:32768
	s_waitcnt lgkmcnt(1)
	v_mfma_f32_16x16x32_f16 v[66:69], v[104:107], v[116:119], v[66:69]
	v_mfma_f32_16x16x32_f16 v[34:37], v[108:111], v[116:119], v[34:37]
	ds_read_b128 v[116:119], v121 offset:34816
	s_waitcnt lgkmcnt(1)
	v_mfma_f32_16x16x32_f16 v[18:21], v[104:107], v[112:115], v[18:21]
	v_mfma_f32_16x16x32_f16 v[2:5], v[108:111], v[112:115], v[2:5]
	ds_read_b128 v[112:115], v121 offset:36864
	s_waitcnt lgkmcnt(1)
	v_mfma_f32_16x16x32_f16 v[26:29], v[104:107], v[116:119], v[26:29]
	v_mfma_f32_16x16x32_f16 v[10:13], v[108:111], v[116:119], v[10:13]
	ds_read_b128 v[116:119], v121 offset:38912
	s_waitcnt lgkmcnt(1)
	v_mfma_f32_16x16x32_f16 v[22:25], v[104:107], v[112:115], v[22:25]
	v_mfma_f32_16x16x32_f16 v[6:9], v[108:111], v[112:115], v[6:9]
	ds_read_b128 v[112:115], v122 offset:16384
	s_waitcnt lgkmcnt(1)
	v_mfma_f32_16x16x32_f16 v[30:33], v[104:107], v[116:119], v[30:33]
	v_mfma_f32_16x16x32_f16 v[14:17], v[108:111], v[116:119], v[14:17]
	ds_read_b128 v[116:119], v122 offset:18432
	ds_read_b128 v[104:107], v94 offset:0
	ds_read_b128 v[108:111], v94 offset:2048
	s_waitcnt lgkmcnt(0)
	v_mfma_f32_16x16x32_f16 v[124:127], v[104:107], v[112:115], v[124:127]
	v_mfma_f32_16x16x32_f16 v[62:65], v[108:111], v[112:115], v[62:65]
	ds_read_b128 v[112:115], v122 offset:20480
	s_waitcnt lgkmcnt(1)
	s_barrier
	s_mov_b32 m0, s24
	s_nop 0
	global_load_lds_dwordx4 v100, s[36:37]
	s_mov_b32 m0, s25
	s_nop 0
	global_load_lds_dwordx4 v101, s[36:37]
	s_mov_b32 m0, s26
	s_nop 0
	global_load_lds_dwordx4 v102, s[36:37]
	s_mov_b32 m0, s27
	s_nop 0
	global_load_lds_dwordx4 v103, s[36:37]
	s_add_u32 s36, s36, 0x80
	s_addc_u32 s37, s37, 0
	s_waitcnt lgkmcnt(1)
	v_mfma_f32_16x16x32_f16 v[86:89], v[104:107], v[116:119], v[86:89]
	v_mfma_f32_16x16x32_f16 v[58:61], v[108:111], v[116:119], v[58:61]
	ds_read_b128 v[116:119], v122 offset:22528
	s_waitcnt lgkmcnt(1)
	v_mfma_f32_16x16x32_f16 v[96:99], v[104:107], v[112:115], v[96:99]
	v_mfma_f32_16x16x32_f16 v[54:57], v[108:111], v[112:115], v[54:57]
	ds_read_b128 v[112:115], v122 offset:24576
	s_waitcnt lgkmcnt(1)
	v_mfma_f32_16x16x32_f16 v[82:85], v[104:107], v[116:119], v[82:85]
	v_mfma_f32_16x16x32_f16 v[50:53], v[108:111], v[116:119], v[50:53]
	ds_read_b128 v[116:119], v122 offset:26624
	s_waitcnt lgkmcnt(1)
	v_mfma_f32_16x16x32_f16 v[78:81], v[104:107], v[112:115], v[78:81]
	v_mfma_f32_16x16x32_f16 v[46:49], v[108:111], v[112:115], v[46:49]
	ds_read_b128 v[112:115], v122 offset:28672
	s_waitcnt lgkmcnt(1)
	v_mfma_f32_16x16x32_f16 v[74:77], v[104:107], v[116:119], v[74:77]
	v_mfma_f32_16x16x32_f16 v[42:45], v[108:111], v[116:119], v[42:45]
	ds_read_b128 v[116:119], v122 offset:30720
	s_waitcnt lgkmcnt(1)
	v_mfma_f32_16x16x32_f16 v[70:73], v[104:107], v[112:115], v[70:73]
	v_mfma_f32_16x16x32_f16 v[38:41], v[108:111], v[112:115], v[38:41]
	ds_read_b128 v[112:115], v122 offset:32768
	s_waitcnt lgkmcnt(1)
	v_mfma_f32_16x16x32_f16 v[66:69], v[104:107], v[116:119], v[66:69]
	v_mfma_f32_16x16x32_f16 v[34:37], v[108:111], v[116:119], v[34:37]
	ds_read_b128 v[116:119], v122 offset:34816
	s_waitcnt lgkmcnt(1)
	v_mfma_f32_16x16x32_f16 v[18:21], v[104:107], v[112:115], v[18:21]
	v_mfma_f32_16x16x32_f16 v[2:5], v[108:111], v[112:115], v[2:5]
	ds_read_b128 v[112:115], v122 offset:36864
	s_waitcnt lgkmcnt(1)
	v_mfma_f32_16x16x32_f16 v[26:29], v[104:107], v[116:119], v[26:29]
	v_mfma_f32_16x16x32_f16 v[10:13], v[108:111], v[116:119], v[10:13]
	ds_read_b128 v[116:119], v122 offset:38912
	s_waitcnt lgkmcnt(0)
	s_barrier
	s_mov_b32 m0, s28
	s_nop 0
	global_load_lds_dwordx4 v120, s[38:39]
	s_mov_b32 m0, s29
	s_nop 0
	global_load_lds_dwordx4 v120, s[46:47]
	s_mov_b32 m0, s30
	s_nop 0
	global_load_lds_dwordx4 v120, s[48:49]
	s_mov_b32 m0, s31
	s_nop 0
	global_load_lds_dwordx4 v120, s[50:51]
	s_mov_b32 m0, s32
	s_nop 0
	global_load_lds_dwordx4 v120, s[52:53]
	s_mov_b32 m0, s33
	s_nop 0
	global_load_lds_dwordx4 v120, s[54:55]
	s_add_u32 s38, s38, 0x80
	s_addc_u32 s39, s39, 0
	s_add_u32 s46, s46, 0x80
	s_addc_u32 s47, s47, 0
	s_add_u32 s48, s48, 0x80
	s_addc_u32 s49, s49, 0
	s_add_u32 s50, s50, 0x80
	s_addc_u32 s51, s51, 0
	s_add_u32 s52, s52, 0x80
	s_addc_u32 s53, s53, 0
	s_add_u32 s54, s54, 0x80
	s_addc_u32 s55, s55, 0
	s_waitcnt lgkmcnt(1)
	v_mfma_f32_16x16x32_f16 v[22:25], v[104:107], v[112:115], v[22:25]
	v_mfma_f32_16x16x32_f16 v[6:9], v[108:111], v[112:115], v[6:9]
	s_waitcnt lgkmcnt(0)
	v_mfma_f32_16x16x32_f16 v[30:33], v[104:107], v[116:119], v[30:33]
	v_mfma_f32_16x16x32_f16 v[14:17], v[108:111], v[116:119], v[14:17]
	s_waitcnt vmcnt(0)
	s_barrier
	ds_read_b128 v[104:107], v93 offset:0
	ds_read_b128 v[108:111], v93 offset:2048
	ds_read_b128 v[112:115], v121 offset:16384
	ds_read_b128 v[116:119], v121 offset:18432
	s_waitcnt lgkmcnt(1)
	v_mfma_f32_16x16x32_f16 v[124:127], v[104:107], v[112:115], v[124:127]
	v_mfma_f32_16x16x32_f16 v[62:65], v[108:111], v[112:115], v[62:65]
	ds_read_b128 v[112:115], v121 offset:20480
	s_waitcnt lgkmcnt(1)
	v_mfma_f32_16x16x32_f16 v[86:89], v[104:107], v[116:119], v[86:89]
	v_mfma_f32_16x16x32_f16 v[58:61], v[108:111], v[116:119], v[58:61]
	ds_read_b128 v[116:119], v121 offset:22528
	s_waitcnt lgkmcnt(1)
	v_mfma_f32_16x16x32_f16 v[96:99], v[104:107], v[112:115], v[96:99]
	v_mfma_f32_16x16x32_f16 v[54:57], v[108:111], v[112:115], v[54:57]
	ds_read_b128 v[112:115], v121 offset:24576
	s_waitcnt lgkmcnt(1)
	v_mfma_f32_16x16x32_f16 v[82:85], v[104:107], v[116:119], v[82:85]
	v_mfma_f32_16x16x32_f16 v[50:53], v[108:111], v[116:119], v[50:53]
	ds_read_b128 v[116:119], v121 offset:26624
	s_waitcnt lgkmcnt(1)
	v_mfma_f32_16x16x32_f16 v[78:81], v[104:107], v[112:115], v[78:81]
	v_mfma_f32_16x16x32_f16 v[46:49], v[108:111], v[112:115], v[46:49]
	ds_read_b128 v[112:115], v121 offset:28672
	s_waitcnt lgkmcnt(1)
	v_mfma_f32_16x16x32_f16 v[74:77], v[104:107], v[116:119], v[74:77]
	v_mfma_f32_16x16x32_f16 v[42:45], v[108:111], v[116:119], v[42:45]
	ds_read_b128 v[116:119], v121 offset:30720
	s_waitcnt lgkmcnt(1)
	v_mfma_f32_16x16x32_f16 v[70:73], v[104:107], v[112:115], v[70:73]
	v_mfma_f32_16x16x32_f16 v[38:41], v[108:111], v[112:115], v[38:41]
	ds_read_b128 v[112:115], v121 offset:32768
	s_waitcnt lgkmcnt(1)
	v_mfma_f32_16x16x32_f16 v[66:69], v[104:107], v[116:119], v[66:69]
	v_mfma_f32_16x16x32_f16 v[34:37], v[108:111], v[116:119], v[34:37]
	ds_read_b128 v[116:119], v121 offset:34816
	s_waitcnt lgkmcnt(1)
	v_mfma_f32_16x16x32_f16 v[18:21], v[104:107], v[112:115], v[18:21]
	v_mfma_f32_16x16x32_f16 v[2:5], v[108:111], v[112:115], v[2:5]
	ds_read_b128 v[112:115], v121 offset:36864
	s_waitcnt lgkmcnt(1)
	v_mfma_f32_16x16x32_f16 v[26:29], v[104:107], v[116:119], v[26:29]
	v_mfma_f32_16x16x32_f16 v[10:13], v[108:111], v[116:119], v[10:13]
	ds_read_b128 v[116:119], v121 offset:38912
	s_waitcnt lgkmcnt(1)
	v_mfma_f32_16x16x32_f16 v[22:25], v[104:107], v[112:115], v[22:25]
	v_mfma_f32_16x16x32_f16 v[6:9], v[108:111], v[112:115], v[6:9]
	ds_read_b128 v[112:115], v122 offset:16384
	s_waitcnt lgkmcnt(1)
	v_mfma_f32_16x16x32_f16 v[30:33], v[104:107], v[116:119], v[30:33]
	v_mfma_f32_16x16x32_f16 v[14:17], v[108:111], v[116:119], v[14:17]
	ds_read_b128 v[116:119], v122 offset:18432
	ds_read_b128 v[104:107], v94 offset:0
	ds_read_b128 v[108:111], v94 offset:2048
	s_waitcnt lgkmcnt(0)
	v_mfma_f32_16x16x32_f16 v[124:127], v[104:107], v[112:115], v[124:127]
	v_mfma_f32_16x16x32_f16 v[62:65], v[108:111], v[112:115], v[62:65]
	ds_read_b128 v[112:115], v122 offset:20480
	s_waitcnt lgkmcnt(1)
	s_barrier
	s_mov_b32 m0, s24
	s_nop 0
	global_load_lds_dwordx4 v100, s[36:37]
	s_mov_b32 m0, s25
	s_nop 0
	global_load_lds_dwordx4 v101, s[36:37]
	s_mov_b32 m0, s26
	s_nop 0
	global_load_lds_dwordx4 v102, s[36:37]
	s_mov_b32 m0, s27
	s_nop 0
	global_load_lds_dwordx4 v103, s[36:37]
	s_add_u32 s36, s36, 0x80
	s_addc_u32 s37, s37, 0
	s_waitcnt lgkmcnt(1)
	v_mfma_f32_16x16x32_f16 v[86:89], v[104:107], v[116:119], v[86:89]
	v_mfma_f32_16x16x32_f16 v[58:61], v[108:111], v[116:119], v[58:61]
	ds_read_b128 v[116:119], v122 offset:22528
	s_waitcnt lgkmcnt(1)
	v_mfma_f32_16x16x32_f16 v[96:99], v[104:107], v[112:115], v[96:99]
	v_mfma_f32_16x16x32_f16 v[54:57], v[108:111], v[112:115], v[54:57]
	ds_read_b128 v[112:115], v122 offset:24576
	s_waitcnt lgkmcnt(1)
	v_mfma_f32_16x16x32_f16 v[82:85], v[104:107], v[116:119], v[82:85]
	v_mfma_f32_16x16x32_f16 v[50:53], v[108:111], v[116:119], v[50:53]
	ds_read_b128 v[116:119], v122 offset:26624
	s_waitcnt lgkmcnt(1)
	v_mfma_f32_16x16x32_f16 v[78:81], v[104:107], v[112:115], v[78:81]
	v_mfma_f32_16x16x32_f16 v[46:49], v[108:111], v[112:115], v[46:49]
	ds_read_b128 v[112:115], v122 offset:28672
	s_waitcnt lgkmcnt(1)
	v_mfma_f32_16x16x32_f16 v[74:77], v[104:107], v[116:119], v[74:77]
	v_mfma_f32_16x16x32_f16 v[42:45], v[108:111], v[116:119], v[42:45]
	ds_read_b128 v[116:119], v122 offset:30720
	s_waitcnt lgkmcnt(1)
	v_mfma_f32_16x16x32_f16 v[70:73], v[104:107], v[112:115], v[70:73]
	v_mfma_f32_16x16x32_f16 v[38:41], v[108:111], v[112:115], v[38:41]
	ds_read_b128 v[112:115], v122 offset:32768
	s_waitcnt lgkmcnt(1)
	v_mfma_f32_16x16x32_f16 v[66:69], v[104:107], v[116:119], v[66:69]
	v_mfma_f32_16x16x32_f16 v[34:37], v[108:111], v[116:119], v[34:37]
	ds_read_b128 v[116:119], v122 offset:34816
	s_waitcnt lgkmcnt(1)
	v_mfma_f32_16x16x32_f16 v[18:21], v[104:107], v[112:115], v[18:21]
	v_mfma_f32_16x16x32_f16 v[2:5], v[108:111], v[112:115], v[2:5]
	ds_read_b128 v[112:115], v122 offset:36864
	s_waitcnt lgkmcnt(1)
	v_mfma_f32_16x16x32_f16 v[26:29], v[104:107], v[116:119], v[26:29]
	v_mfma_f32_16x16x32_f16 v[10:13], v[108:111], v[116:119], v[10:13]
	ds_read_b128 v[116:119], v122 offset:38912
	s_waitcnt lgkmcnt(0)
	s_barrier
	s_mov_b32 m0, s28
	s_nop 0
	global_load_lds_dwordx4 v120, s[38:39]
	s_mov_b32 m0, s29
	s_nop 0
	global_load_lds_dwordx4 v120, s[46:47]
	s_mov_b32 m0, s30
	s_nop 0
	global_load_lds_dwordx4 v120, s[48:49]
	s_mov_b32 m0, s31
	s_nop 0
	global_load_lds_dwordx4 v120, s[50:51]
	s_mov_b32 m0, s32
	s_nop 0
	global_load_lds_dwordx4 v120, s[52:53]
	s_mov_b32 m0, s33
	s_nop 0
	global_load_lds_dwordx4 v120, s[54:55]
	s_add_u32 s38, s38, 0x80
	s_addc_u32 s39, s39, 0
	s_add_u32 s46, s46, 0x80
	s_addc_u32 s47, s47, 0
	s_add_u32 s48, s48, 0x80
	s_addc_u32 s49, s49, 0
	s_add_u32 s50, s50, 0x80
	s_addc_u32 s51, s51, 0
	s_add_u32 s52, s52, 0x80
	s_addc_u32 s53, s53, 0
	s_add_u32 s54, s54, 0x80
	s_addc_u32 s55, s55, 0
	s_waitcnt lgkmcnt(1)
	v_mfma_f32_16x16x32_f16 v[22:25], v[104:107], v[112:115], v[22:25]
	v_mfma_f32_16x16x32_f16 v[6:9], v[108:111], v[112:115], v[6:9]
	s_waitcnt lgkmcnt(0)
	v_mfma_f32_16x16x32_f16 v[30:33], v[104:107], v[116:119], v[30:33]
	v_mfma_f32_16x16x32_f16 v[14:17], v[108:111], v[116:119], v[14:17]
	s_waitcnt vmcnt(0)
	s_barrier
	ds_read_b128 v[104:107], v93 offset:0
	ds_read_b128 v[108:111], v93 offset:2048
	ds_read_b128 v[112:115], v121 offset:16384
	ds_read_b128 v[116:119], v121 offset:18432
	s_waitcnt lgkmcnt(1)
	v_mfma_f32_16x16x32_f16 v[124:127], v[104:107], v[112:115], v[124:127]
	v_mfma_f32_16x16x32_f16 v[62:65], v[108:111], v[112:115], v[62:65]
	ds_read_b128 v[112:115], v121 offset:20480
	s_waitcnt lgkmcnt(1)
	v_mfma_f32_16x16x32_f16 v[86:89], v[104:107], v[116:119], v[86:89]
	v_mfma_f32_16x16x32_f16 v[58:61], v[108:111], v[116:119], v[58:61]
	ds_read_b128 v[116:119], v121 offset:22528
	s_waitcnt lgkmcnt(1)
	v_mfma_f32_16x16x32_f16 v[96:99], v[104:107], v[112:115], v[96:99]
	v_mfma_f32_16x16x32_f16 v[54:57], v[108:111], v[112:115], v[54:57]
	ds_read_b128 v[112:115], v121 offset:24576
	s_waitcnt lgkmcnt(1)
	v_mfma_f32_16x16x32_f16 v[82:85], v[104:107], v[116:119], v[82:85]
	v_mfma_f32_16x16x32_f16 v[50:53], v[108:111], v[116:119], v[50:53]
	ds_read_b128 v[116:119], v121 offset:26624
	s_waitcnt lgkmcnt(1)
	v_mfma_f32_16x16x32_f16 v[78:81], v[104:107], v[112:115], v[78:81]
	v_mfma_f32_16x16x32_f16 v[46:49], v[108:111], v[112:115], v[46:49]
	ds_read_b128 v[112:115], v121 offset:28672
	s_waitcnt lgkmcnt(1)
	v_mfma_f32_16x16x32_f16 v[74:77], v[104:107], v[116:119], v[74:77]
	v_mfma_f32_16x16x32_f16 v[42:45], v[108:111], v[116:119], v[42:45]
	ds_read_b128 v[116:119], v121 offset:30720
	s_waitcnt lgkmcnt(1)
	v_mfma_f32_16x16x32_f16 v[70:73], v[104:107], v[112:115], v[70:73]
	v_mfma_f32_16x16x32_f16 v[38:41], v[108:111], v[112:115], v[38:41]
	ds_read_b128 v[112:115], v121 offset:32768
	s_waitcnt lgkmcnt(1)
	v_mfma_f32_16x16x32_f16 v[66:69], v[104:107], v[116:119], v[66:69]
	v_mfma_f32_16x16x32_f16 v[34:37], v[108:111], v[116:119], v[34:37]
	ds_read_b128 v[116:119], v121 offset:34816
	s_waitcnt lgkmcnt(1)
	v_mfma_f32_16x16x32_f16 v[18:21], v[104:107], v[112:115], v[18:21]
	v_mfma_f32_16x16x32_f16 v[2:5], v[108:111], v[112:115], v[2:5]
	ds_read_b128 v[112:115], v121 offset:36864
	s_waitcnt lgkmcnt(1)
	v_mfma_f32_16x16x32_f16 v[26:29], v[104:107], v[116:119], v[26:29]
	v_mfma_f32_16x16x32_f16 v[10:13], v[108:111], v[116:119], v[10:13]
	ds_read_b128 v[116:119], v121 offset:38912
	s_waitcnt lgkmcnt(1)
	v_mfma_f32_16x16x32_f16 v[22:25], v[104:107], v[112:115], v[22:25]
	v_mfma_f32_16x16x32_f16 v[6:9], v[108:111], v[112:115], v[6:9]
	ds_read_b128 v[112:115], v122 offset:16384
	s_waitcnt lgkmcnt(1)
	v_mfma_f32_16x16x32_f16 v[30:33], v[104:107], v[116:119], v[30:33]
	v_mfma_f32_16x16x32_f16 v[14:17], v[108:111], v[116:119], v[14:17]
	ds_read_b128 v[116:119], v122 offset:18432
	ds_read_b128 v[104:107], v94 offset:0
	ds_read_b128 v[108:111], v94 offset:2048
	s_waitcnt lgkmcnt(0)
	v_mfma_f32_16x16x32_f16 v[124:127], v[104:107], v[112:115], v[124:127]
	v_mfma_f32_16x16x32_f16 v[62:65], v[108:111], v[112:115], v[62:65]
	ds_read_b128 v[112:115], v122 offset:20480
	s_waitcnt lgkmcnt(1)
	s_barrier
	s_mov_b32 m0, s24
	s_nop 0
	global_load_lds_dwordx4 v100, s[36:37]
	s_mov_b32 m0, s25
	s_nop 0
	global_load_lds_dwordx4 v101, s[36:37]
	s_mov_b32 m0, s26
	s_nop 0
	global_load_lds_dwordx4 v102, s[36:37]
	s_mov_b32 m0, s27
	s_nop 0
	global_load_lds_dwordx4 v103, s[36:37]
	s_add_u32 s36, s36, 0x80
	s_addc_u32 s37, s37, 0
	s_waitcnt lgkmcnt(1)
	v_mfma_f32_16x16x32_f16 v[86:89], v[104:107], v[116:119], v[86:89]
	v_mfma_f32_16x16x32_f16 v[58:61], v[108:111], v[116:119], v[58:61]
	ds_read_b128 v[116:119], v122 offset:22528
	s_waitcnt lgkmcnt(1)
	v_mfma_f32_16x16x32_f16 v[96:99], v[104:107], v[112:115], v[96:99]
	v_mfma_f32_16x16x32_f16 v[54:57], v[108:111], v[112:115], v[54:57]
	ds_read_b128 v[112:115], v122 offset:24576
	s_waitcnt lgkmcnt(1)
	v_mfma_f32_16x16x32_f16 v[82:85], v[104:107], v[116:119], v[82:85]
	v_mfma_f32_16x16x32_f16 v[50:53], v[108:111], v[116:119], v[50:53]
	ds_read_b128 v[116:119], v122 offset:26624
	s_waitcnt lgkmcnt(1)
	v_mfma_f32_16x16x32_f16 v[78:81], v[104:107], v[112:115], v[78:81]
	v_mfma_f32_16x16x32_f16 v[46:49], v[108:111], v[112:115], v[46:49]
	ds_read_b128 v[112:115], v122 offset:28672
	s_waitcnt lgkmcnt(1)
	v_mfma_f32_16x16x32_f16 v[74:77], v[104:107], v[116:119], v[74:77]
	v_mfma_f32_16x16x32_f16 v[42:45], v[108:111], v[116:119], v[42:45]
	ds_read_b128 v[116:119], v122 offset:30720
	s_waitcnt lgkmcnt(1)
	v_mfma_f32_16x16x32_f16 v[70:73], v[104:107], v[112:115], v[70:73]
	v_mfma_f32_16x16x32_f16 v[38:41], v[108:111], v[112:115], v[38:41]
	ds_read_b128 v[112:115], v122 offset:32768
	s_waitcnt lgkmcnt(1)
	v_mfma_f32_16x16x32_f16 v[66:69], v[104:107], v[116:119], v[66:69]
	v_mfma_f32_16x16x32_f16 v[34:37], v[108:111], v[116:119], v[34:37]
	ds_read_b128 v[116:119], v122 offset:34816
	s_waitcnt lgkmcnt(1)
	v_mfma_f32_16x16x32_f16 v[18:21], v[104:107], v[112:115], v[18:21]
	v_mfma_f32_16x16x32_f16 v[2:5], v[108:111], v[112:115], v[2:5]
	ds_read_b128 v[112:115], v122 offset:36864
	s_waitcnt lgkmcnt(1)
	v_mfma_f32_16x16x32_f16 v[26:29], v[104:107], v[116:119], v[26:29]
	v_mfma_f32_16x16x32_f16 v[10:13], v[108:111], v[116:119], v[10:13]
	ds_read_b128 v[116:119], v122 offset:38912
	s_waitcnt lgkmcnt(0)
	s_barrier
	s_mov_b32 m0, s28
	s_nop 0
	global_load_lds_dwordx4 v120, s[38:39]
	s_mov_b32 m0, s29
	s_nop 0
	global_load_lds_dwordx4 v120, s[46:47]
	s_mov_b32 m0, s30
	s_nop 0
	global_load_lds_dwordx4 v120, s[48:49]
	s_mov_b32 m0, s31
	s_nop 0
	global_load_lds_dwordx4 v120, s[50:51]
	s_mov_b32 m0, s32
	s_nop 0
	global_load_lds_dwordx4 v120, s[52:53]
	s_mov_b32 m0, s33
	s_nop 0
	global_load_lds_dwordx4 v120, s[54:55]
	s_add_u32 s38, s38, 0x80
	s_addc_u32 s39, s39, 0
	s_add_u32 s46, s46, 0x80
	s_addc_u32 s47, s47, 0
	s_add_u32 s48, s48, 0x80
	s_addc_u32 s49, s49, 0
	s_add_u32 s50, s50, 0x80
	s_addc_u32 s51, s51, 0
	s_add_u32 s52, s52, 0x80
	s_addc_u32 s53, s53, 0
	s_add_u32 s54, s54, 0x80
	s_addc_u32 s55, s55, 0
	s_waitcnt lgkmcnt(1)
	v_mfma_f32_16x16x32_f16 v[22:25], v[104:107], v[112:115], v[22:25]
	v_mfma_f32_16x16x32_f16 v[6:9], v[108:111], v[112:115], v[6:9]
	s_waitcnt lgkmcnt(0)
	v_mfma_f32_16x16x32_f16 v[30:33], v[104:107], v[116:119], v[30:33]
	v_mfma_f32_16x16x32_f16 v[14:17], v[108:111], v[116:119], v[14:17]
	s_waitcnt vmcnt(0)
	s_barrier
	ds_read_b128 v[104:107], v93 offset:0
	ds_read_b128 v[108:111], v93 offset:2048
	ds_read_b128 v[112:115], v121 offset:16384
	ds_read_b128 v[116:119], v121 offset:18432
	s_waitcnt lgkmcnt(1)
	v_mfma_f32_16x16x32_f16 v[124:127], v[104:107], v[112:115], v[124:127]
	v_mfma_f32_16x16x32_f16 v[62:65], v[108:111], v[112:115], v[62:65]
	ds_read_b128 v[112:115], v121 offset:20480
	s_waitcnt lgkmcnt(1)
	v_mfma_f32_16x16x32_f16 v[86:89], v[104:107], v[116:119], v[86:89]
	v_mfma_f32_16x16x32_f16 v[58:61], v[108:111], v[116:119], v[58:61]
	ds_read_b128 v[116:119], v121 offset:22528
	s_waitcnt lgkmcnt(1)
	v_mfma_f32_16x16x32_f16 v[96:99], v[104:107], v[112:115], v[96:99]
	v_mfma_f32_16x16x32_f16 v[54:57], v[108:111], v[112:115], v[54:57]
	ds_read_b128 v[112:115], v121 offset:24576
	s_waitcnt lgkmcnt(1)
	v_mfma_f32_16x16x32_f16 v[82:85], v[104:107], v[116:119], v[82:85]
	v_mfma_f32_16x16x32_f16 v[50:53], v[108:111], v[116:119], v[50:53]
	ds_read_b128 v[116:119], v121 offset:26624
	s_waitcnt lgkmcnt(1)
	v_mfma_f32_16x16x32_f16 v[78:81], v[104:107], v[112:115], v[78:81]
	v_mfma_f32_16x16x32_f16 v[46:49], v[108:111], v[112:115], v[46:49]
	ds_read_b128 v[112:115], v121 offset:28672
	s_waitcnt lgkmcnt(1)
	v_mfma_f32_16x16x32_f16 v[74:77], v[104:107], v[116:119], v[74:77]
	v_mfma_f32_16x16x32_f16 v[42:45], v[108:111], v[116:119], v[42:45]
	ds_read_b128 v[116:119], v121 offset:30720
	s_waitcnt lgkmcnt(1)
	v_mfma_f32_16x16x32_f16 v[70:73], v[104:107], v[112:115], v[70:73]
	v_mfma_f32_16x16x32_f16 v[38:41], v[108:111], v[112:115], v[38:41]
	ds_read_b128 v[112:115], v121 offset:32768
	s_waitcnt lgkmcnt(1)
	v_mfma_f32_16x16x32_f16 v[66:69], v[104:107], v[116:119], v[66:69]
	v_mfma_f32_16x16x32_f16 v[34:37], v[108:111], v[116:119], v[34:37]
	ds_read_b128 v[116:119], v121 offset:34816
	s_waitcnt lgkmcnt(1)
	v_mfma_f32_16x16x32_f16 v[18:21], v[104:107], v[112:115], v[18:21]
	v_mfma_f32_16x16x32_f16 v[2:5], v[108:111], v[112:115], v[2:5]
	ds_read_b128 v[112:115], v121 offset:36864
	s_waitcnt lgkmcnt(1)
	v_mfma_f32_16x16x32_f16 v[26:29], v[104:107], v[116:119], v[26:29]
	v_mfma_f32_16x16x32_f16 v[10:13], v[108:111], v[116:119], v[10:13]
	ds_read_b128 v[116:119], v121 offset:38912
	s_waitcnt lgkmcnt(1)
	v_mfma_f32_16x16x32_f16 v[22:25], v[104:107], v[112:115], v[22:25]
	v_mfma_f32_16x16x32_f16 v[6:9], v[108:111], v[112:115], v[6:9]
	ds_read_b128 v[112:115], v122 offset:16384
	s_waitcnt lgkmcnt(1)
	v_mfma_f32_16x16x32_f16 v[30:33], v[104:107], v[116:119], v[30:33]
	v_mfma_f32_16x16x32_f16 v[14:17], v[108:111], v[116:119], v[14:17]
	ds_read_b128 v[116:119], v122 offset:18432
	ds_read_b128 v[104:107], v94 offset:0
	ds_read_b128 v[108:111], v94 offset:2048
	s_waitcnt lgkmcnt(0)
	v_mfma_f32_16x16x32_f16 v[124:127], v[104:107], v[112:115], v[124:127]
	v_mfma_f32_16x16x32_f16 v[62:65], v[108:111], v[112:115], v[62:65]
	ds_read_b128 v[112:115], v122 offset:20480
	s_waitcnt lgkmcnt(1)
	s_barrier
	s_mov_b32 m0, s24
	s_nop 0
	global_load_lds_dwordx4 v100, s[36:37]
	s_mov_b32 m0, s25
	s_nop 0
	global_load_lds_dwordx4 v101, s[36:37]
	s_mov_b32 m0, s26
	s_nop 0
	global_load_lds_dwordx4 v102, s[36:37]
	s_mov_b32 m0, s27
	s_nop 0
	global_load_lds_dwordx4 v103, s[36:37]
	s_add_u32 s36, s36, 0x80
	s_addc_u32 s37, s37, 0
	s_waitcnt lgkmcnt(1)
	v_mfma_f32_16x16x32_f16 v[86:89], v[104:107], v[116:119], v[86:89]
	v_mfma_f32_16x16x32_f16 v[58:61], v[108:111], v[116:119], v[58:61]
	ds_read_b128 v[116:119], v122 offset:22528
	s_waitcnt lgkmcnt(1)
	v_mfma_f32_16x16x32_f16 v[96:99], v[104:107], v[112:115], v[96:99]
	v_mfma_f32_16x16x32_f16 v[54:57], v[108:111], v[112:115], v[54:57]
	ds_read_b128 v[112:115], v122 offset:24576
	s_waitcnt lgkmcnt(1)
	v_mfma_f32_16x16x32_f16 v[82:85], v[104:107], v[116:119], v[82:85]
	v_mfma_f32_16x16x32_f16 v[50:53], v[108:111], v[116:119], v[50:53]
	ds_read_b128 v[116:119], v122 offset:26624
	s_waitcnt lgkmcnt(1)
	v_mfma_f32_16x16x32_f16 v[78:81], v[104:107], v[112:115], v[78:81]
	v_mfma_f32_16x16x32_f16 v[46:49], v[108:111], v[112:115], v[46:49]
	ds_read_b128 v[112:115], v122 offset:28672
	s_waitcnt lgkmcnt(1)
	v_mfma_f32_16x16x32_f16 v[74:77], v[104:107], v[116:119], v[74:77]
	v_mfma_f32_16x16x32_f16 v[42:45], v[108:111], v[116:119], v[42:45]
	ds_read_b128 v[116:119], v122 offset:30720
	s_waitcnt lgkmcnt(1)
	v_mfma_f32_16x16x32_f16 v[70:73], v[104:107], v[112:115], v[70:73]
	v_mfma_f32_16x16x32_f16 v[38:41], v[108:111], v[112:115], v[38:41]
	ds_read_b128 v[112:115], v122 offset:32768
	s_waitcnt lgkmcnt(1)
	v_mfma_f32_16x16x32_f16 v[66:69], v[104:107], v[116:119], v[66:69]
	v_mfma_f32_16x16x32_f16 v[34:37], v[108:111], v[116:119], v[34:37]
	ds_read_b128 v[116:119], v122 offset:34816
	s_waitcnt lgkmcnt(1)
	v_mfma_f32_16x16x32_f16 v[18:21], v[104:107], v[112:115], v[18:21]
	v_mfma_f32_16x16x32_f16 v[2:5], v[108:111], v[112:115], v[2:5]
	ds_read_b128 v[112:115], v122 offset:36864
	s_waitcnt lgkmcnt(1)
	v_mfma_f32_16x16x32_f16 v[26:29], v[104:107], v[116:119], v[26:29]
	v_mfma_f32_16x16x32_f16 v[10:13], v[108:111], v[116:119], v[10:13]
	ds_read_b128 v[116:119], v122 offset:38912
	s_waitcnt lgkmcnt(0)
	s_barrier
	s_mov_b32 m0, s28
	s_nop 0
	global_load_lds_dwordx4 v120, s[38:39]
	s_mov_b32 m0, s29
	s_nop 0
	global_load_lds_dwordx4 v120, s[46:47]
	s_mov_b32 m0, s30
	s_nop 0
	global_load_lds_dwordx4 v120, s[48:49]
	s_mov_b32 m0, s31
	s_nop 0
	global_load_lds_dwordx4 v120, s[50:51]
	s_mov_b32 m0, s32
	s_nop 0
	global_load_lds_dwordx4 v120, s[52:53]
	s_mov_b32 m0, s33
	s_nop 0
	global_load_lds_dwordx4 v120, s[54:55]
	s_add_u32 s38, s38, 0x80
	s_addc_u32 s39, s39, 0
	s_add_u32 s46, s46, 0x80
	s_addc_u32 s47, s47, 0
	s_add_u32 s48, s48, 0x80
	s_addc_u32 s49, s49, 0
	s_add_u32 s50, s50, 0x80
	s_addc_u32 s51, s51, 0
	s_add_u32 s52, s52, 0x80
	s_addc_u32 s53, s53, 0
	s_add_u32 s54, s54, 0x80
	s_addc_u32 s55, s55, 0
	s_waitcnt lgkmcnt(1)
	v_mfma_f32_16x16x32_f16 v[22:25], v[104:107], v[112:115], v[22:25]
	v_mfma_f32_16x16x32_f16 v[6:9], v[108:111], v[112:115], v[6:9]
	s_waitcnt lgkmcnt(0)
	v_mfma_f32_16x16x32_f16 v[30:33], v[104:107], v[116:119], v[30:33]
	v_mfma_f32_16x16x32_f16 v[14:17], v[108:111], v[116:119], v[14:17]
	s_waitcnt vmcnt(0)
	s_barrier
	ds_read_b128 v[104:107], v93 offset:0
	ds_read_b128 v[108:111], v93 offset:2048
	ds_read_b128 v[112:115], v121 offset:16384
	ds_read_b128 v[116:119], v121 offset:18432
	s_waitcnt lgkmcnt(1)
	v_mfma_f32_16x16x32_f16 v[124:127], v[104:107], v[112:115], v[124:127]
	v_mfma_f32_16x16x32_f16 v[62:65], v[108:111], v[112:115], v[62:65]
	ds_read_b128 v[112:115], v121 offset:20480
	s_waitcnt lgkmcnt(1)
	v_mfma_f32_16x16x32_f16 v[86:89], v[104:107], v[116:119], v[86:89]
	v_mfma_f32_16x16x32_f16 v[58:61], v[108:111], v[116:119], v[58:61]
	ds_read_b128 v[116:119], v121 offset:22528
	s_waitcnt lgkmcnt(1)
	v_mfma_f32_16x16x32_f16 v[96:99], v[104:107], v[112:115], v[96:99]
	v_mfma_f32_16x16x32_f16 v[54:57], v[108:111], v[112:115], v[54:57]
	ds_read_b128 v[112:115], v121 offset:24576
	s_waitcnt lgkmcnt(1)
	v_mfma_f32_16x16x32_f16 v[82:85], v[104:107], v[116:119], v[82:85]
	v_mfma_f32_16x16x32_f16 v[50:53], v[108:111], v[116:119], v[50:53]
	ds_read_b128 v[116:119], v121 offset:26624
	s_waitcnt lgkmcnt(1)
	v_mfma_f32_16x16x32_f16 v[78:81], v[104:107], v[112:115], v[78:81]
	v_mfma_f32_16x16x32_f16 v[46:49], v[108:111], v[112:115], v[46:49]
	ds_read_b128 v[112:115], v121 offset:28672
	s_waitcnt lgkmcnt(1)
	v_mfma_f32_16x16x32_f16 v[74:77], v[104:107], v[116:119], v[74:77]
	v_mfma_f32_16x16x32_f16 v[42:45], v[108:111], v[116:119], v[42:45]
	ds_read_b128 v[116:119], v121 offset:30720
	s_waitcnt lgkmcnt(1)
	v_mfma_f32_16x16x32_f16 v[70:73], v[104:107], v[112:115], v[70:73]
	v_mfma_f32_16x16x32_f16 v[38:41], v[108:111], v[112:115], v[38:41]
	ds_read_b128 v[112:115], v121 offset:32768
	s_waitcnt lgkmcnt(1)
	v_mfma_f32_16x16x32_f16 v[66:69], v[104:107], v[116:119], v[66:69]
	v_mfma_f32_16x16x32_f16 v[34:37], v[108:111], v[116:119], v[34:37]
	ds_read_b128 v[116:119], v121 offset:34816
	s_waitcnt lgkmcnt(1)
	v_mfma_f32_16x16x32_f16 v[18:21], v[104:107], v[112:115], v[18:21]
	v_mfma_f32_16x16x32_f16 v[2:5], v[108:111], v[112:115], v[2:5]
	ds_read_b128 v[112:115], v121 offset:36864
	s_waitcnt lgkmcnt(1)
	v_mfma_f32_16x16x32_f16 v[26:29], v[104:107], v[116:119], v[26:29]
	v_mfma_f32_16x16x32_f16 v[10:13], v[108:111], v[116:119], v[10:13]
	ds_read_b128 v[116:119], v121 offset:38912
	s_waitcnt lgkmcnt(1)
	v_mfma_f32_16x16x32_f16 v[22:25], v[104:107], v[112:115], v[22:25]
	v_mfma_f32_16x16x32_f16 v[6:9], v[108:111], v[112:115], v[6:9]
	ds_read_b128 v[112:115], v122 offset:16384
	s_waitcnt lgkmcnt(1)
	v_mfma_f32_16x16x32_f16 v[30:33], v[104:107], v[116:119], v[30:33]
	v_mfma_f32_16x16x32_f16 v[14:17], v[108:111], v[116:119], v[14:17]
	ds_read_b128 v[116:119], v122 offset:18432
	ds_read_b128 v[104:107], v94 offset:0
	ds_read_b128 v[108:111], v94 offset:2048
	s_waitcnt lgkmcnt(0)
	v_mfma_f32_16x16x32_f16 v[124:127], v[104:107], v[112:115], v[124:127]
	v_mfma_f32_16x16x32_f16 v[62:65], v[108:111], v[112:115], v[62:65]
	ds_read_b128 v[112:115], v122 offset:20480
	s_waitcnt lgkmcnt(1)
	s_barrier
	s_mov_b32 m0, s24
	s_nop 0
	global_load_lds_dwordx4 v100, s[36:37]
	s_mov_b32 m0, s25
	s_nop 0
	global_load_lds_dwordx4 v101, s[36:37]
	s_mov_b32 m0, s26
	s_nop 0
	global_load_lds_dwordx4 v102, s[36:37]
	s_mov_b32 m0, s27
	s_nop 0
	global_load_lds_dwordx4 v103, s[36:37]
	s_add_u32 s36, s36, 0x80
	s_addc_u32 s37, s37, 0
	s_waitcnt lgkmcnt(1)
	v_mfma_f32_16x16x32_f16 v[86:89], v[104:107], v[116:119], v[86:89]
	v_mfma_f32_16x16x32_f16 v[58:61], v[108:111], v[116:119], v[58:61]
	ds_read_b128 v[116:119], v122 offset:22528
	s_waitcnt lgkmcnt(1)
	v_mfma_f32_16x16x32_f16 v[96:99], v[104:107], v[112:115], v[96:99]
	v_mfma_f32_16x16x32_f16 v[54:57], v[108:111], v[112:115], v[54:57]
	ds_read_b128 v[112:115], v122 offset:24576
	s_waitcnt lgkmcnt(1)
	v_mfma_f32_16x16x32_f16 v[82:85], v[104:107], v[116:119], v[82:85]
	v_mfma_f32_16x16x32_f16 v[50:53], v[108:111], v[116:119], v[50:53]
	ds_read_b128 v[116:119], v122 offset:26624
	s_waitcnt lgkmcnt(1)
	v_mfma_f32_16x16x32_f16 v[78:81], v[104:107], v[112:115], v[78:81]
	v_mfma_f32_16x16x32_f16 v[46:49], v[108:111], v[112:115], v[46:49]
	ds_read_b128 v[112:115], v122 offset:28672
	s_waitcnt lgkmcnt(1)
	v_mfma_f32_16x16x32_f16 v[74:77], v[104:107], v[116:119], v[74:77]
	v_mfma_f32_16x16x32_f16 v[42:45], v[108:111], v[116:119], v[42:45]
	ds_read_b128 v[116:119], v122 offset:30720
	s_waitcnt lgkmcnt(1)
	v_mfma_f32_16x16x32_f16 v[70:73], v[104:107], v[112:115], v[70:73]
	v_mfma_f32_16x16x32_f16 v[38:41], v[108:111], v[112:115], v[38:41]
	ds_read_b128 v[112:115], v122 offset:32768
	s_waitcnt lgkmcnt(1)
	v_mfma_f32_16x16x32_f16 v[66:69], v[104:107], v[116:119], v[66:69]
	v_mfma_f32_16x16x32_f16 v[34:37], v[108:111], v[116:119], v[34:37]
	ds_read_b128 v[116:119], v122 offset:34816
	s_waitcnt lgkmcnt(1)
	v_mfma_f32_16x16x32_f16 v[18:21], v[104:107], v[112:115], v[18:21]
	v_mfma_f32_16x16x32_f16 v[2:5], v[108:111], v[112:115], v[2:5]
	ds_read_b128 v[112:115], v122 offset:36864
	s_waitcnt lgkmcnt(1)
	v_mfma_f32_16x16x32_f16 v[26:29], v[104:107], v[116:119], v[26:29]
	v_mfma_f32_16x16x32_f16 v[10:13], v[108:111], v[116:119], v[10:13]
	ds_read_b128 v[116:119], v122 offset:38912
	s_waitcnt lgkmcnt(0)
	s_barrier
	s_mov_b32 m0, s28
	s_nop 0
	global_load_lds_dwordx4 v120, s[38:39]
	s_mov_b32 m0, s29
	s_nop 0
	global_load_lds_dwordx4 v120, s[46:47]
	s_mov_b32 m0, s30
	s_nop 0
	global_load_lds_dwordx4 v120, s[48:49]
	s_mov_b32 m0, s31
	s_nop 0
	global_load_lds_dwordx4 v120, s[50:51]
	s_mov_b32 m0, s32
	s_nop 0
	global_load_lds_dwordx4 v120, s[52:53]
	s_mov_b32 m0, s33
	s_nop 0
	global_load_lds_dwordx4 v120, s[54:55]
	s_add_u32 s38, s38, 0x80
	s_addc_u32 s39, s39, 0
	s_add_u32 s46, s46, 0x80
	s_addc_u32 s47, s47, 0
	s_add_u32 s48, s48, 0x80
	s_addc_u32 s49, s49, 0
	s_add_u32 s50, s50, 0x80
	s_addc_u32 s51, s51, 0
	s_add_u32 s52, s52, 0x80
	s_addc_u32 s53, s53, 0
	s_add_u32 s54, s54, 0x80
	s_addc_u32 s55, s55, 0
	s_waitcnt lgkmcnt(1)
	v_mfma_f32_16x16x32_f16 v[22:25], v[104:107], v[112:115], v[22:25]
	v_mfma_f32_16x16x32_f16 v[6:9], v[108:111], v[112:115], v[6:9]
	s_waitcnt lgkmcnt(0)
	v_mfma_f32_16x16x32_f16 v[30:33], v[104:107], v[116:119], v[30:33]
	v_mfma_f32_16x16x32_f16 v[14:17], v[108:111], v[116:119], v[14:17]
	s_waitcnt vmcnt(0)
	s_barrier
	ds_read_b128 v[104:107], v93 offset:0
	ds_read_b128 v[108:111], v93 offset:2048
	ds_read_b128 v[112:115], v121 offset:16384
	ds_read_b128 v[116:119], v121 offset:18432
	s_waitcnt lgkmcnt(1)
	v_mfma_f32_16x16x32_f16 v[124:127], v[104:107], v[112:115], v[124:127]
	v_mfma_f32_16x16x32_f16 v[62:65], v[108:111], v[112:115], v[62:65]
	ds_read_b128 v[112:115], v121 offset:20480
	s_waitcnt lgkmcnt(1)
	v_mfma_f32_16x16x32_f16 v[86:89], v[104:107], v[116:119], v[86:89]
	v_mfma_f32_16x16x32_f16 v[58:61], v[108:111], v[116:119], v[58:61]
	ds_read_b128 v[116:119], v121 offset:22528
	s_waitcnt lgkmcnt(1)
	v_mfma_f32_16x16x32_f16 v[96:99], v[104:107], v[112:115], v[96:99]
	v_mfma_f32_16x16x32_f16 v[54:57], v[108:111], v[112:115], v[54:57]
	ds_read_b128 v[112:115], v121 offset:24576
	s_waitcnt lgkmcnt(1)
	v_mfma_f32_16x16x32_f16 v[82:85], v[104:107], v[116:119], v[82:85]
	v_mfma_f32_16x16x32_f16 v[50:53], v[108:111], v[116:119], v[50:53]
	ds_read_b128 v[116:119], v121 offset:26624
	s_waitcnt lgkmcnt(1)
	v_mfma_f32_16x16x32_f16 v[78:81], v[104:107], v[112:115], v[78:81]
	v_mfma_f32_16x16x32_f16 v[46:49], v[108:111], v[112:115], v[46:49]
	ds_read_b128 v[112:115], v121 offset:28672
	s_waitcnt lgkmcnt(1)
	v_mfma_f32_16x16x32_f16 v[74:77], v[104:107], v[116:119], v[74:77]
	v_mfma_f32_16x16x32_f16 v[42:45], v[108:111], v[116:119], v[42:45]
	ds_read_b128 v[116:119], v121 offset:30720
	s_waitcnt lgkmcnt(1)
	v_mfma_f32_16x16x32_f16 v[70:73], v[104:107], v[112:115], v[70:73]
	v_mfma_f32_16x16x32_f16 v[38:41], v[108:111], v[112:115], v[38:41]
	ds_read_b128 v[112:115], v121 offset:32768
	s_waitcnt lgkmcnt(1)
	v_mfma_f32_16x16x32_f16 v[66:69], v[104:107], v[116:119], v[66:69]
	v_mfma_f32_16x16x32_f16 v[34:37], v[108:111], v[116:119], v[34:37]
	ds_read_b128 v[116:119], v121 offset:34816
	s_waitcnt lgkmcnt(1)
	v_mfma_f32_16x16x32_f16 v[18:21], v[104:107], v[112:115], v[18:21]
	v_mfma_f32_16x16x32_f16 v[2:5], v[108:111], v[112:115], v[2:5]
	ds_read_b128 v[112:115], v121 offset:36864
	s_waitcnt lgkmcnt(1)
	v_mfma_f32_16x16x32_f16 v[26:29], v[104:107], v[116:119], v[26:29]
	v_mfma_f32_16x16x32_f16 v[10:13], v[108:111], v[116:119], v[10:13]
	ds_read_b128 v[116:119], v121 offset:38912
	s_waitcnt lgkmcnt(1)
	v_mfma_f32_16x16x32_f16 v[22:25], v[104:107], v[112:115], v[22:25]
	v_mfma_f32_16x16x32_f16 v[6:9], v[108:111], v[112:115], v[6:9]
	ds_read_b128 v[112:115], v122 offset:16384
	s_waitcnt lgkmcnt(1)
	v_mfma_f32_16x16x32_f16 v[30:33], v[104:107], v[116:119], v[30:33]
	v_mfma_f32_16x16x32_f16 v[14:17], v[108:111], v[116:119], v[14:17]
	ds_read_b128 v[116:119], v122 offset:18432
	ds_read_b128 v[104:107], v94 offset:0
	ds_read_b128 v[108:111], v94 offset:2048
	s_waitcnt lgkmcnt(0)
	v_mfma_f32_16x16x32_f16 v[124:127], v[104:107], v[112:115], v[124:127]
	v_mfma_f32_16x16x32_f16 v[62:65], v[108:111], v[112:115], v[62:65]
	ds_read_b128 v[112:115], v122 offset:20480
	s_waitcnt lgkmcnt(1)
	s_barrier
	s_mov_b32 m0, s24
	s_nop 0
	global_load_lds_dwordx4 v100, s[36:37]
	s_mov_b32 m0, s25
	s_nop 0
	global_load_lds_dwordx4 v101, s[36:37]
	s_mov_b32 m0, s26
	s_nop 0
	global_load_lds_dwordx4 v102, s[36:37]
	s_mov_b32 m0, s27
	s_nop 0
	global_load_lds_dwordx4 v103, s[36:37]
	s_add_u32 s36, s36, 0x80
	s_addc_u32 s37, s37, 0
	s_waitcnt lgkmcnt(1)
	v_mfma_f32_16x16x32_f16 v[86:89], v[104:107], v[116:119], v[86:89]
	v_mfma_f32_16x16x32_f16 v[58:61], v[108:111], v[116:119], v[58:61]
	ds_read_b128 v[116:119], v122 offset:22528
	s_waitcnt lgkmcnt(1)
	v_mfma_f32_16x16x32_f16 v[96:99], v[104:107], v[112:115], v[96:99]
	v_mfma_f32_16x16x32_f16 v[54:57], v[108:111], v[112:115], v[54:57]
	ds_read_b128 v[112:115], v122 offset:24576
	s_waitcnt lgkmcnt(1)
	v_mfma_f32_16x16x32_f16 v[82:85], v[104:107], v[116:119], v[82:85]
	v_mfma_f32_16x16x32_f16 v[50:53], v[108:111], v[116:119], v[50:53]
	ds_read_b128 v[116:119], v122 offset:26624
	s_waitcnt lgkmcnt(1)
	v_mfma_f32_16x16x32_f16 v[78:81], v[104:107], v[112:115], v[78:81]
	v_mfma_f32_16x16x32_f16 v[46:49], v[108:111], v[112:115], v[46:49]
	ds_read_b128 v[112:115], v122 offset:28672
	s_waitcnt lgkmcnt(1)
	v_mfma_f32_16x16x32_f16 v[74:77], v[104:107], v[116:119], v[74:77]
	v_mfma_f32_16x16x32_f16 v[42:45], v[108:111], v[116:119], v[42:45]
	ds_read_b128 v[116:119], v122 offset:30720
	s_waitcnt lgkmcnt(1)
	v_mfma_f32_16x16x32_f16 v[70:73], v[104:107], v[112:115], v[70:73]
	v_mfma_f32_16x16x32_f16 v[38:41], v[108:111], v[112:115], v[38:41]
	ds_read_b128 v[112:115], v122 offset:32768
	s_waitcnt lgkmcnt(1)
	v_mfma_f32_16x16x32_f16 v[66:69], v[104:107], v[116:119], v[66:69]
	v_mfma_f32_16x16x32_f16 v[34:37], v[108:111], v[116:119], v[34:37]
	ds_read_b128 v[116:119], v122 offset:34816
	s_waitcnt lgkmcnt(1)
	v_mfma_f32_16x16x32_f16 v[18:21], v[104:107], v[112:115], v[18:21]
	v_mfma_f32_16x16x32_f16 v[2:5], v[108:111], v[112:115], v[2:5]
	ds_read_b128 v[112:115], v122 offset:36864
	s_waitcnt lgkmcnt(1)
	v_mfma_f32_16x16x32_f16 v[26:29], v[104:107], v[116:119], v[26:29]
	v_mfma_f32_16x16x32_f16 v[10:13], v[108:111], v[116:119], v[10:13]
	ds_read_b128 v[116:119], v122 offset:38912
	s_waitcnt lgkmcnt(0)
	s_barrier
	s_mov_b32 m0, s28
	s_nop 0
	global_load_lds_dwordx4 v120, s[38:39]
	s_mov_b32 m0, s29
	s_nop 0
	global_load_lds_dwordx4 v120, s[46:47]
	s_mov_b32 m0, s30
	s_nop 0
	global_load_lds_dwordx4 v120, s[48:49]
	s_mov_b32 m0, s31
	s_nop 0
	global_load_lds_dwordx4 v120, s[50:51]
	s_mov_b32 m0, s32
	s_nop 0
	global_load_lds_dwordx4 v120, s[52:53]
	s_mov_b32 m0, s33
	s_nop 0
	global_load_lds_dwordx4 v120, s[54:55]
	s_add_u32 s38, s38, 0x80
	s_addc_u32 s39, s39, 0
	s_add_u32 s46, s46, 0x80
	s_addc_u32 s47, s47, 0
	s_add_u32 s48, s48, 0x80
	s_addc_u32 s49, s49, 0
	s_add_u32 s50, s50, 0x80
	s_addc_u32 s51, s51, 0
	s_add_u32 s52, s52, 0x80
	s_addc_u32 s53, s53, 0
	s_add_u32 s54, s54, 0x80
	s_addc_u32 s55, s55, 0
	s_waitcnt lgkmcnt(1)
	v_mfma_f32_16x16x32_f16 v[22:25], v[104:107], v[112:115], v[22:25]
	v_mfma_f32_16x16x32_f16 v[6:9], v[108:111], v[112:115], v[6:9]
	s_waitcnt lgkmcnt(0)
	v_mfma_f32_16x16x32_f16 v[30:33], v[104:107], v[116:119], v[30:33]
	v_mfma_f32_16x16x32_f16 v[14:17], v[108:111], v[116:119], v[14:17]
	s_waitcnt vmcnt(0)
	s_barrier
	ds_read_b128 v[104:107], v93 offset:0
	ds_read_b128 v[108:111], v93 offset:2048
	ds_read_b128 v[112:115], v121 offset:16384
	ds_read_b128 v[116:119], v121 offset:18432
	s_waitcnt lgkmcnt(1)
	v_mfma_f32_16x16x32_f16 v[124:127], v[104:107], v[112:115], v[124:127]
	v_mfma_f32_16x16x32_f16 v[62:65], v[108:111], v[112:115], v[62:65]
	ds_read_b128 v[112:115], v121 offset:20480
	s_waitcnt lgkmcnt(1)
	v_mfma_f32_16x16x32_f16 v[86:89], v[104:107], v[116:119], v[86:89]
	v_mfma_f32_16x16x32_f16 v[58:61], v[108:111], v[116:119], v[58:61]
	ds_read_b128 v[116:119], v121 offset:22528
	s_waitcnt lgkmcnt(1)
	v_mfma_f32_16x16x32_f16 v[96:99], v[104:107], v[112:115], v[96:99]
	v_mfma_f32_16x16x32_f16 v[54:57], v[108:111], v[112:115], v[54:57]
	ds_read_b128 v[112:115], v121 offset:24576
	s_waitcnt lgkmcnt(1)
	v_mfma_f32_16x16x32_f16 v[82:85], v[104:107], v[116:119], v[82:85]
	v_mfma_f32_16x16x32_f16 v[50:53], v[108:111], v[116:119], v[50:53]
	ds_read_b128 v[116:119], v121 offset:26624
	s_waitcnt lgkmcnt(1)
	v_mfma_f32_16x16x32_f16 v[78:81], v[104:107], v[112:115], v[78:81]
	v_mfma_f32_16x16x32_f16 v[46:49], v[108:111], v[112:115], v[46:49]
	ds_read_b128 v[112:115], v121 offset:28672
	s_waitcnt lgkmcnt(1)
	v_mfma_f32_16x16x32_f16 v[74:77], v[104:107], v[116:119], v[74:77]
	v_mfma_f32_16x16x32_f16 v[42:45], v[108:111], v[116:119], v[42:45]
	ds_read_b128 v[116:119], v121 offset:30720
	s_waitcnt lgkmcnt(1)
	v_mfma_f32_16x16x32_f16 v[70:73], v[104:107], v[112:115], v[70:73]
	v_mfma_f32_16x16x32_f16 v[38:41], v[108:111], v[112:115], v[38:41]
	ds_read_b128 v[112:115], v121 offset:32768
	s_waitcnt lgkmcnt(1)
	v_mfma_f32_16x16x32_f16 v[66:69], v[104:107], v[116:119], v[66:69]
	v_mfma_f32_16x16x32_f16 v[34:37], v[108:111], v[116:119], v[34:37]
	ds_read_b128 v[116:119], v121 offset:34816
	s_waitcnt lgkmcnt(1)
	v_mfma_f32_16x16x32_f16 v[18:21], v[104:107], v[112:115], v[18:21]
	v_mfma_f32_16x16x32_f16 v[2:5], v[108:111], v[112:115], v[2:5]
	ds_read_b128 v[112:115], v121 offset:36864
	s_waitcnt lgkmcnt(1)
	v_mfma_f32_16x16x32_f16 v[26:29], v[104:107], v[116:119], v[26:29]
	v_mfma_f32_16x16x32_f16 v[10:13], v[108:111], v[116:119], v[10:13]
	ds_read_b128 v[116:119], v121 offset:38912
	s_waitcnt lgkmcnt(1)
	v_mfma_f32_16x16x32_f16 v[22:25], v[104:107], v[112:115], v[22:25]
	v_mfma_f32_16x16x32_f16 v[6:9], v[108:111], v[112:115], v[6:9]
	ds_read_b128 v[112:115], v122 offset:16384
	s_waitcnt lgkmcnt(1)
	v_mfma_f32_16x16x32_f16 v[30:33], v[104:107], v[116:119], v[30:33]
	v_mfma_f32_16x16x32_f16 v[14:17], v[108:111], v[116:119], v[14:17]
	ds_read_b128 v[116:119], v122 offset:18432
	ds_read_b128 v[104:107], v94 offset:0
	ds_read_b128 v[108:111], v94 offset:2048
	s_waitcnt lgkmcnt(0)
	v_mfma_f32_16x16x32_f16 v[124:127], v[104:107], v[112:115], v[124:127]
	v_mfma_f32_16x16x32_f16 v[62:65], v[108:111], v[112:115], v[62:65]
	ds_read_b128 v[112:115], v122 offset:20480
	s_waitcnt lgkmcnt(1)
	s_barrier
	s_mov_b32 m0, s24
	s_nop 0
	global_load_lds_dwordx4 v100, s[36:37]
	s_mov_b32 m0, s25
	s_nop 0
	global_load_lds_dwordx4 v101, s[36:37]
	s_mov_b32 m0, s26
	s_nop 0
	global_load_lds_dwordx4 v102, s[36:37]
	s_mov_b32 m0, s27
	s_nop 0
	global_load_lds_dwordx4 v103, s[36:37]
	s_add_u32 s36, s36, 0x80
	s_addc_u32 s37, s37, 0
	s_waitcnt lgkmcnt(1)
	v_mfma_f32_16x16x32_f16 v[86:89], v[104:107], v[116:119], v[86:89]
	v_mfma_f32_16x16x32_f16 v[58:61], v[108:111], v[116:119], v[58:61]
	ds_read_b128 v[116:119], v122 offset:22528
	s_waitcnt lgkmcnt(1)
	v_mfma_f32_16x16x32_f16 v[96:99], v[104:107], v[112:115], v[96:99]
	v_mfma_f32_16x16x32_f16 v[54:57], v[108:111], v[112:115], v[54:57]
	ds_read_b128 v[112:115], v122 offset:24576
	s_waitcnt lgkmcnt(1)
	v_mfma_f32_16x16x32_f16 v[82:85], v[104:107], v[116:119], v[82:85]
	v_mfma_f32_16x16x32_f16 v[50:53], v[108:111], v[116:119], v[50:53]
	ds_read_b128 v[116:119], v122 offset:26624
	s_waitcnt lgkmcnt(1)
	v_mfma_f32_16x16x32_f16 v[78:81], v[104:107], v[112:115], v[78:81]
	v_mfma_f32_16x16x32_f16 v[46:49], v[108:111], v[112:115], v[46:49]
	ds_read_b128 v[112:115], v122 offset:28672
	s_waitcnt lgkmcnt(1)
	v_mfma_f32_16x16x32_f16 v[74:77], v[104:107], v[116:119], v[74:77]
	v_mfma_f32_16x16x32_f16 v[42:45], v[108:111], v[116:119], v[42:45]
	ds_read_b128 v[116:119], v122 offset:30720
	s_waitcnt lgkmcnt(1)
	v_mfma_f32_16x16x32_f16 v[70:73], v[104:107], v[112:115], v[70:73]
	v_mfma_f32_16x16x32_f16 v[38:41], v[108:111], v[112:115], v[38:41]
	ds_read_b128 v[112:115], v122 offset:32768
	s_waitcnt lgkmcnt(1)
	v_mfma_f32_16x16x32_f16 v[66:69], v[104:107], v[116:119], v[66:69]
	v_mfma_f32_16x16x32_f16 v[34:37], v[108:111], v[116:119], v[34:37]
	ds_read_b128 v[116:119], v122 offset:34816
	s_waitcnt lgkmcnt(1)
	v_mfma_f32_16x16x32_f16 v[18:21], v[104:107], v[112:115], v[18:21]
	v_mfma_f32_16x16x32_f16 v[2:5], v[108:111], v[112:115], v[2:5]
	ds_read_b128 v[112:115], v122 offset:36864
	s_waitcnt lgkmcnt(1)
	v_mfma_f32_16x16x32_f16 v[26:29], v[104:107], v[116:119], v[26:29]
	v_mfma_f32_16x16x32_f16 v[10:13], v[108:111], v[116:119], v[10:13]
	ds_read_b128 v[116:119], v122 offset:38912
	s_waitcnt lgkmcnt(0)
	s_barrier
	s_mov_b32 m0, s28
	s_nop 0
	global_load_lds_dwordx4 v120, s[38:39]
	s_mov_b32 m0, s29
	s_nop 0
	global_load_lds_dwordx4 v120, s[46:47]
	s_mov_b32 m0, s30
	s_nop 0
	global_load_lds_dwordx4 v120, s[48:49]
	s_mov_b32 m0, s31
	s_nop 0
	global_load_lds_dwordx4 v120, s[50:51]
	s_mov_b32 m0, s32
	s_nop 0
	global_load_lds_dwordx4 v120, s[52:53]
	s_mov_b32 m0, s33
	s_nop 0
	global_load_lds_dwordx4 v120, s[54:55]
	s_add_u32 s38, s38, 0x80
	s_addc_u32 s39, s39, 0
	s_add_u32 s46, s46, 0x80
	s_addc_u32 s47, s47, 0
	s_add_u32 s48, s48, 0x80
	s_addc_u32 s49, s49, 0
	s_add_u32 s50, s50, 0x80
	s_addc_u32 s51, s51, 0
	s_add_u32 s52, s52, 0x80
	s_addc_u32 s53, s53, 0
	s_add_u32 s54, s54, 0x80
	s_addc_u32 s55, s55, 0
	s_waitcnt lgkmcnt(1)
	v_mfma_f32_16x16x32_f16 v[22:25], v[104:107], v[112:115], v[22:25]
	v_mfma_f32_16x16x32_f16 v[6:9], v[108:111], v[112:115], v[6:9]
	s_waitcnt lgkmcnt(0)
	v_mfma_f32_16x16x32_f16 v[30:33], v[104:107], v[116:119], v[30:33]
	v_mfma_f32_16x16x32_f16 v[14:17], v[108:111], v[116:119], v[14:17]
	s_waitcnt vmcnt(0)
	s_barrier
	ds_read_b128 v[104:107], v93 offset:0
	ds_read_b128 v[108:111], v93 offset:2048
	ds_read_b128 v[112:115], v121 offset:16384
	ds_read_b128 v[116:119], v121 offset:18432
	s_waitcnt lgkmcnt(1)
	v_mfma_f32_16x16x32_f16 v[124:127], v[104:107], v[112:115], v[124:127]
	v_mfma_f32_16x16x32_f16 v[62:65], v[108:111], v[112:115], v[62:65]
	ds_read_b128 v[112:115], v121 offset:20480
	s_waitcnt lgkmcnt(1)
	v_mfma_f32_16x16x32_f16 v[86:89], v[104:107], v[116:119], v[86:89]
	v_mfma_f32_16x16x32_f16 v[58:61], v[108:111], v[116:119], v[58:61]
	ds_read_b128 v[116:119], v121 offset:22528
	s_waitcnt lgkmcnt(1)
	v_mfma_f32_16x16x32_f16 v[96:99], v[104:107], v[112:115], v[96:99]
	v_mfma_f32_16x16x32_f16 v[54:57], v[108:111], v[112:115], v[54:57]
	ds_read_b128 v[112:115], v121 offset:24576
	s_waitcnt lgkmcnt(1)
	v_mfma_f32_16x16x32_f16 v[82:85], v[104:107], v[116:119], v[82:85]
	v_mfma_f32_16x16x32_f16 v[50:53], v[108:111], v[116:119], v[50:53]
	ds_read_b128 v[116:119], v121 offset:26624
	s_waitcnt lgkmcnt(1)
	v_mfma_f32_16x16x32_f16 v[78:81], v[104:107], v[112:115], v[78:81]
	v_mfma_f32_16x16x32_f16 v[46:49], v[108:111], v[112:115], v[46:49]
	ds_read_b128 v[112:115], v121 offset:28672
	s_waitcnt lgkmcnt(1)
	v_mfma_f32_16x16x32_f16 v[74:77], v[104:107], v[116:119], v[74:77]
	v_mfma_f32_16x16x32_f16 v[42:45], v[108:111], v[116:119], v[42:45]
	ds_read_b128 v[116:119], v121 offset:30720
	s_waitcnt lgkmcnt(1)
	v_mfma_f32_16x16x32_f16 v[70:73], v[104:107], v[112:115], v[70:73]
	v_mfma_f32_16x16x32_f16 v[38:41], v[108:111], v[112:115], v[38:41]
	ds_read_b128 v[112:115], v121 offset:32768
	s_waitcnt lgkmcnt(1)
	v_mfma_f32_16x16x32_f16 v[66:69], v[104:107], v[116:119], v[66:69]
	v_mfma_f32_16x16x32_f16 v[34:37], v[108:111], v[116:119], v[34:37]
	ds_read_b128 v[116:119], v121 offset:34816
	s_waitcnt lgkmcnt(1)
	v_mfma_f32_16x16x32_f16 v[18:21], v[104:107], v[112:115], v[18:21]
	v_mfma_f32_16x16x32_f16 v[2:5], v[108:111], v[112:115], v[2:5]
	ds_read_b128 v[112:115], v121 offset:36864
	s_waitcnt lgkmcnt(1)
	v_mfma_f32_16x16x32_f16 v[26:29], v[104:107], v[116:119], v[26:29]
	v_mfma_f32_16x16x32_f16 v[10:13], v[108:111], v[116:119], v[10:13]
	ds_read_b128 v[116:119], v121 offset:38912
	s_waitcnt lgkmcnt(1)
	v_mfma_f32_16x16x32_f16 v[22:25], v[104:107], v[112:115], v[22:25]
	v_mfma_f32_16x16x32_f16 v[6:9], v[108:111], v[112:115], v[6:9]
	ds_read_b128 v[112:115], v122 offset:16384
	s_waitcnt lgkmcnt(1)
	v_mfma_f32_16x16x32_f16 v[30:33], v[104:107], v[116:119], v[30:33]
	v_mfma_f32_16x16x32_f16 v[14:17], v[108:111], v[116:119], v[14:17]
	ds_read_b128 v[116:119], v122 offset:18432
	ds_read_b128 v[104:107], v94 offset:0
	ds_read_b128 v[108:111], v94 offset:2048
	s_waitcnt lgkmcnt(0)
	v_mfma_f32_16x16x32_f16 v[124:127], v[104:107], v[112:115], v[124:127]
	v_mfma_f32_16x16x32_f16 v[62:65], v[108:111], v[112:115], v[62:65]
	ds_read_b128 v[112:115], v122 offset:20480
	s_waitcnt lgkmcnt(1)
	v_mfma_f32_16x16x32_f16 v[86:89], v[104:107], v[116:119], v[86:89]
	v_mfma_f32_16x16x32_f16 v[58:61], v[108:111], v[116:119], v[58:61]
	ds_read_b128 v[116:119], v122 offset:22528
	s_waitcnt lgkmcnt(1)
	v_mfma_f32_16x16x32_f16 v[96:99], v[104:107], v[112:115], v[96:99]
	v_mfma_f32_16x16x32_f16 v[54:57], v[108:111], v[112:115], v[54:57]
	ds_read_b128 v[112:115], v122 offset:24576
	s_waitcnt lgkmcnt(1)
	v_mfma_f32_16x16x32_f16 v[82:85], v[104:107], v[116:119], v[82:85]
	v_mfma_f32_16x16x32_f16 v[50:53], v[108:111], v[116:119], v[50:53]
	ds_read_b128 v[116:119], v122 offset:26624
	s_waitcnt lgkmcnt(1)
	v_mfma_f32_16x16x32_f16 v[78:81], v[104:107], v[112:115], v[78:81]
	v_mfma_f32_16x16x32_f16 v[46:49], v[108:111], v[112:115], v[46:49]
	ds_read_b128 v[112:115], v122 offset:28672
	s_waitcnt lgkmcnt(1)
	v_mfma_f32_16x16x32_f16 v[74:77], v[104:107], v[116:119], v[74:77]
	v_mfma_f32_16x16x32_f16 v[42:45], v[108:111], v[116:119], v[42:45]
	ds_read_b128 v[116:119], v122 offset:30720
	s_waitcnt lgkmcnt(1)
	v_mfma_f32_16x16x32_f16 v[70:73], v[104:107], v[112:115], v[70:73]
	v_mfma_f32_16x16x32_f16 v[38:41], v[108:111], v[112:115], v[38:41]
	ds_read_b128 v[112:115], v122 offset:32768
	s_waitcnt lgkmcnt(1)
	v_mfma_f32_16x16x32_f16 v[66:69], v[104:107], v[116:119], v[66:69]
	v_mfma_f32_16x16x32_f16 v[34:37], v[108:111], v[116:119], v[34:37]
	ds_read_b128 v[116:119], v122 offset:34816
	s_waitcnt lgkmcnt(1)
	v_mfma_f32_16x16x32_f16 v[18:21], v[104:107], v[112:115], v[18:21]
	v_mfma_f32_16x16x32_f16 v[2:5], v[108:111], v[112:115], v[2:5]
	ds_read_b128 v[112:115], v122 offset:36864
	s_waitcnt lgkmcnt(1)
	v_mfma_f32_16x16x32_f16 v[26:29], v[104:107], v[116:119], v[26:29]
	v_mfma_f32_16x16x32_f16 v[10:13], v[108:111], v[116:119], v[10:13]
	ds_read_b128 v[116:119], v122 offset:38912
	s_waitcnt lgkmcnt(0)
	s_barrier
	s_waitcnt lgkmcnt(1)
	v_mfma_f32_16x16x32_f16 v[22:25], v[104:107], v[112:115], v[22:25]
	v_mfma_f32_16x16x32_f16 v[6:9], v[108:111], v[112:115], v[6:9]
	s_waitcnt lgkmcnt(0)
	v_mfma_f32_16x16x32_f16 v[30:33], v[104:107], v[116:119], v[30:33]
	v_mfma_f32_16x16x32_f16 v[14:17], v[108:111], v[116:119], v[14:17]
	s_nop 15
	s_nop 15
	s_movk_i32 s2, 0xfc
	v_cmp_gt_u32_e32 vcc, s2, v0
	s_mov_b32 s2, 0x12492493
	s_movk_i32 s4, 0x380
	s_movk_i32 s12, 0x110
	v_cmp_gt_u32_e64 s[4:5], s4, v0
	v_lshrrev_b32_e32 v93, 1, v0
	v_cndmask_b32_e32 v94, 0, v93, vcc
	s_nop 5
	v_cvt_f16_f32_e32 v86, v86
	s_nop 5
	v_cvt_f16_f32_e32 v54, v54
	v_cvt_f16_f32_e32 v82, v82
	v_cvt_f16_f32_e32 v50, v50
	s_nop 5
	v_cvt_f16_f32_e32 v78, v78
	v_mul_i32_i24_e32 v102, 0xffffffc2, v92
	v_mul_u32_u24_e32 v101, 0x110, v91
	v_lshlrev_b32_e32 v91, 6, v92
	v_add3_u32 v91, v91, v102, v101
	ds_write_b16 v91, v86 offset:32
	v_cvt_f16_f32_e32 v86, v87
	v_cvt_f16_f32_e32 v74, v74
	v_cvt_f16_f32_e32 v102, v125
	ds_write_b16 v91, v86 offset:304
	v_cvt_f16_f32_e32 v86, v88
	s_nop 2
	v_cvt_f16_f32_e32 v34, v34
	ds_write_b16 v91, v82 offset:96
	ds_write_b16 v91, v86 offset:576
	v_cvt_f16_f32_e32 v86, v89
	v_cvt_f16_f32_e32 v38, v38
	ds_write_b16 v91, v34 offset:4576
	ds_write_b16 v91, v86 offset:848
	v_cvt_f16_f32_e32 v86, v96
	s_nop 1
	v_cvt_f16_f32_e32 v62, v62
	v_cvt_f16_f32_e32 v34, v35
	s_nop 0
	v_cvt_f16_f32_e32 v58, v58
	ds_write_b16 v91, v38 offset:4544
	v_cvt_f16_f32_e32 v38, v39
	s_nop 1
	v_cvt_f16_f32_e32 v46, v46
	ds_write_b16 v91, v86 offset:64
	v_cvt_f16_f32_e32 v86, v97
	s_nop 0
	v_cvt_f16_f32_e32 v42, v42
	v_cvt_f16_f32_e32 v82, v83
	ds_write_b16 v91, v78 offset:128
	s_nop 1
	v_cvt_f16_f32_e32 v70, v70
	v_cvt_f16_f32_e32 v78, v79
	ds_write_b16 v91, v74 offset:160
	v_cvt_f16_f32_e32 v74, v75
	s_nop 0
	v_cvt_f16_f32_e32 v66, v66
	ds_write_b16 v91, v70 offset:192
	v_cvt_f16_f32_e32 v70, v71
	ds_write_b16 v91, v62 offset:4352
	ds_write_b16 v91, v66 offset:224
	v_cvt_f16_f32_e32 v66, v67
	v_cvt_f16_f32_e32 v62, v63
	ds_write_b16 v91, v58 offset:4384
	v_cvt_f16_f32_e32 v58, v59
	ds_write_b16 v91, v54 offset:4416
	v_cvt_f16_f32_e32 v54, v55
	ds_write_b16 v91, v50 offset:4448
	v_cvt_f16_f32_e32 v50, v51
	ds_write_b16 v91, v46 offset:4480
	v_cvt_f16_f32_e32 v46, v47
	ds_write_b16 v91, v42 offset:4512
	v_cvt_f16_f32_e32 v42, v43
	ds_write_b16 v91, v34 offset:4848
	v_cvt_f16_f32_e32 v34, v36
	ds_write_b16 v91, v38 offset:4816
	v_cvt_f16_f32_e32 v38, v40
	ds_write_b16 v91, v102 offset:272
	v_cvt_f16_f32_e32 v102, v126
	ds_write_b16 v91, v86 offset:336
	v_cvt_f16_f32_e32 v86, v98
	ds_write_b16 v91, v82 offset:368
	v_cvt_f16_f32_e32 v82, v84
	ds_write_b16 v91, v78 offset:400
	v_cvt_f16_f32_e32 v78, v80
	ds_write_b16 v91, v74 offset:432
	v_cvt_f16_f32_e32 v74, v76
	ds_write_b16 v91, v70 offset:464
	v_cvt_f16_f32_e32 v70, v72
	ds_write_b16 v91, v66 offset:496
	v_cvt_f16_f32_e32 v66, v68
	ds_write_b16 v91, v62 offset:4624
	v_cvt_f16_f32_e32 v62, v64
	ds_write_b16 v91, v58 offset:4656
	v_cvt_f16_f32_e32 v58, v60
	ds_write_b16 v91, v54 offset:4688
	v_cvt_f16_f32_e32 v54, v56
	ds_write_b16 v91, v50 offset:4720
	v_cvt_f16_f32_e32 v50, v52
	ds_write_b16 v91, v46 offset:4752
	v_cvt_f16_f32_e32 v46, v48
	ds_write_b16 v91, v42 offset:4784
	v_cvt_f16_f32_e32 v42, v44
	ds_write_b16 v91, v34 offset:5120
	v_cvt_f16_f32_e32 v34, v37
	ds_write_b16 v91, v38 offset:5088
	v_cvt_f16_f32_e32 v38, v41
	v_cvt_f16_f32_e32 v103, v124
	ds_write_b16 v91, v102 offset:544
	v_cvt_f16_f32_e32 v102, v127
	ds_write_b16 v91, v86 offset:608
	v_cvt_f16_f32_e32 v86, v99
	ds_write_b16 v91, v82 offset:640
	v_cvt_f16_f32_e32 v82, v85
	ds_write_b16 v91, v78 offset:672
	v_cvt_f16_f32_e32 v78, v81
	ds_write_b16 v91, v74 offset:704
	v_cvt_f16_f32_e32 v74, v77
	ds_write_b16 v91, v70 offset:736
	v_cvt_f16_f32_e32 v70, v73
	ds_write_b16 v91, v66 offset:768
	v_cvt_f16_f32_e32 v66, v69
	ds_write_b16 v91, v62 offset:4896
	v_cvt_f16_f32_e32 v62, v65
	ds_write_b16 v91, v58 offset:4928
	v_cvt_f16_f32_e32 v58, v61
	ds_write_b16 v91, v54 offset:4960
	v_cvt_f16_f32_e32 v54, v57
	ds_write_b16 v91, v50 offset:4992
	v_cvt_f16_f32_e32 v50, v53
	ds_write_b16 v91, v46 offset:5024
	v_cvt_f16_f32_e32 v46, v49
	ds_write_b16 v91, v42 offset:5056
	v_cvt_f16_f32_e32 v42, v45
	ds_write_b16 v91, v34 offset:5392
	v_min_u32_e32 v34, 8, v92
	v_mul_hi_u32 v100, v94, s2
	ds_write_b16 v91, v38 offset:5360
	v_cmp_gt_u32_e64 s[2:3], 9, v92
	v_mul_u32_u24_e32 v39, 14, v34
	v_and_b32_e32 v40, 48, v0
	v_lshlrev_b32_e32 v38, 2, v92
	ds_write_b16 v91, v103
	ds_write_b16 v91, v102 offset:816
	ds_write_b16 v91, v86 offset:880
	ds_write_b16 v91, v82 offset:912
	ds_write_b16 v91, v78 offset:944
	ds_write_b16 v91, v74 offset:976
	ds_write_b16 v91, v70 offset:1008
	ds_write_b16 v91, v66 offset:1040
	ds_write_b16 v91, v62 offset:5168
	ds_write_b16 v91, v58 offset:5200
	ds_write_b16 v91, v54 offset:5232
	ds_write_b16 v91, v50 offset:5264
	ds_write_b16 v91, v46 offset:5296
	ds_write_b16 v91, v42 offset:5328
	s_waitcnt lgkmcnt(0)
	s_barrier
	s_and_saveexec_b64 s[6:7], s[4:5]
	s_cbranch_execz .LBB1_9
	v_add_u32_e32 v34, v1, v39
	v_mad_u32_u24 v41, v34, s12, v40
	ds_read_b128 v[34:37], v41
	ds_read_b128 v[42:45], v41 offset:64
	ds_read_b128 v[46:49], v41 offset:128
	ds_read_b128 v[50:53], v41 offset:192
	v_cmp_ne_u32_e64 s[4:5], 3, v90
	v_mul_u32_u24_e32 v41, 9, v1
	s_and_b64 s[12:13], s[4:5], s[2:3]
	s_waitcnt lgkmcnt(1)
	v_mfma_f32_16x16x32_f16 v[34:37], v[34:37], v[46:49], 0
	s_waitcnt lgkmcnt(0)
	v_mfma_f32_16x16x32_f16 v[34:37], v[42:45], v[50:53], v[34:37]
	s_and_saveexec_b64 s[4:5], s[12:13]
	v_add_u32_e32 v42, v95, v41
	s_nop 5
	v_mul_f32_e32 v34, 0x3e000000, v34
	v_mad_u32_u24 v42, v42, 48, v38
	ds_write_b32 v42, v34 offset:34816
	s_or_b64 exec, exec, s[4:5]
	v_or_b32_e32 v34, 1, v95
	v_cmp_gt_u32_e64 s[4:5], 9, v34
	s_and_b64 s[12:13], s[4:5], s[2:3]
	s_and_saveexec_b64 s[4:5], s[12:13]
	v_add_u32_e32 v34, v34, v41
	v_mul_f32_e32 v35, 0x3e000000, v35
	v_mad_u32_u24 v34, v34, 48, v38
	ds_write_b32 v34, v35 offset:34816
	s_or_b64 exec, exec, s[4:5]
	v_or_b32_e32 v34, 2, v95
	v_cmp_gt_u32_e64 s[4:5], 9, v34
	s_and_b64 s[12:13], s[4:5], s[2:3]
	s_and_saveexec_b64 s[4:5], s[12:13]
	v_add_u32_e32 v34, v34, v41
	v_mul_f32_e32 v35, 0x3e000000, v36
	v_mad_u32_u24 v34, v34, 48, v38
	ds_write_b32 v34, v35 offset:34816
	s_or_b64 exec, exec, s[4:5]
	v_or_b32_e32 v34, 3, v95
	v_cmp_gt_u32_e64 s[4:5], 9, v34
	s_and_b64 s[4:5], s[4:5], s[2:3]
	s_and_b64 exec, exec, s[4:5]
	v_add_u32_e32 v34, v34, v41
	v_mul_f32_e32 v35, 0x3e000000, v37
	v_mad_u32_u24 v34, v34, 48, v38
	ds_write_b32 v34, v35 offset:34816
.LBB1_9:
	s_or_b64 exec, exec, s[6:7]
	s_load_dwordx4 s[12:15], s[0:1], 0x18
	s_load_dwordx2 s[6:7], s[0:1], 0x28
	v_mul_i32_i24_e32 v41, -14, v100
	s_movk_i32 s0, 0x280
	v_cmp_gt_u32_e64 s[0:1], s0, v0
	s_mov_b64 s[4:5], exec
	s_and_b64 s[0:1], s[4:5], s[0:1]
	v_lshrrev_b32_e32 v64, 3, v0
	s_mov_b64 exec, s[0:1]
	s_cbranch_execz .LBB1_18
	v_or_b32_e32 v54, 4, v1
	v_add_u32_e32 v34, v54, v39
	s_movk_i32 s0, 0x110
	v_mad_u32_u24 v50, v34, s0, v40
	ds_read_b128 v[34:37], v50
	ds_read_b128 v[42:45], v50 offset:64
	ds_read_b128 v[46:49], v50 offset:128
	ds_read_b128 v[50:53], v50 offset:192
	v_cmp_ne_u32_e64 s[0:1], 3, v90
	s_and_b64 s[18:19], s[0:1], s[2:3]
	s_waitcnt lgkmcnt(0)
	v_mfma_f32_16x16x32_f16 v[34:37], v[34:37], v[46:49], 0
	v_mfma_f32_16x16x32_f16 v[34:37], v[42:45], v[50:53], v[34:37]
	v_mul_u32_u24_e32 v42, 9, v54
	s_and_saveexec_b64 s[0:1], s[18:19]
	v_add_u32_e32 v43, v95, v42
	s_nop 4
	v_mul_f32_e32 v34, 0x3e000000, v34
	v_mad_u32_u24 v43, v43, 48, v38
	ds_write_b32 v43, v34 offset:34816
	s_or_b64 exec, exec, s[0:1]
	v_or_b32_e32 v34, 1, v95
	v_cmp_gt_u32_e64 s[0:1], 9, v34
	s_and_b64 s[18:19], s[0:1], s[2:3]
	s_and_saveexec_b64 s[0:1], s[18:19]
	v_add_u32_e32 v34, v34, v42
	v_mul_f32_e32 v35, 0x3e000000, v35
	v_mad_u32_u24 v34, v34, 48, v38
	ds_write_b32 v34, v35 offset:34816
	s_or_b64 exec, exec, s[0:1]
	v_or_b32_e32 v34, 2, v95
	v_cmp_gt_u32_e64 s[0:1], 9, v34
	s_and_b64 s[18:19], s[0:1], s[2:3]
	s_and_saveexec_b64 s[0:1], s[18:19]
	v_add_u32_e32 v34, v34, v42
	v_mul_f32_e32 v35, 0x3e000000, v36
	v_mad_u32_u24 v34, v34, 48, v38
	ds_write_b32 v34, v35 offset:34816
	s_or_b64 exec, exec, s[0:1]
	v_or_b32_e32 v34, 3, v95
	v_cmp_gt_u32_e64 s[0:1], 9, v34
	s_and_b64 s[0:1], s[0:1], s[2:3]
	s_and_b64 exec, exec, s[0:1]
	v_add_u32_e32 v34, v34, v42
	v_mul_f32_e32 v35, 0x3e000000, v37
	v_mad_u32_u24 v34, v34, 48, v38
	ds_write_b32 v34, v35 offset:34816
.LBB1_18:
	s_or_b64 exec, exec, s[4:5]
	s_movk_i32 s0, 0x180
	v_cmp_gt_u32_e64 s[0:1], s0, v0
	s_and_saveexec_b64 s[4:5], s[0:1]
	s_cbranch_execz .LBB1_27
	v_or_b32_e32 v54, 8, v1
	v_add_u32_e32 v34, v54, v39
	s_movk_i32 s0, 0x110
	v_mad_u32_u24 v50, v34, s0, v40
	ds_read_b128 v[34:37], v50
	ds_read_b128 v[42:45], v50 offset:64
	ds_read_b128 v[46:49], v50 offset:128
	ds_read_b128 v[50:53], v50 offset:192
	v_cmp_ne_u32_e64 s[0:1], 3, v90
	s_and_b64 s[18:19], s[0:1], s[2:3]
	s_waitcnt lgkmcnt(0)
	v_mfma_f32_16x16x32_f16 v[34:37], v[34:37], v[46:49], 0
	v_mfma_f32_16x16x32_f16 v[34:37], v[42:45], v[50:53], v[34:37]
	v_mul_u32_u24_e32 v42, 9, v54
	s_and_saveexec_b64 s[0:1], s[18:19]
	v_add_u32_e32 v43, v95, v42
	s_nop 4
	v_mul_f32_e32 v34, 0x3e000000, v34
	v_mad_u32_u24 v43, v43, 48, v38
	ds_write_b32 v43, v34 offset:34816
	s_or_b64 exec, exec, s[0:1]
	v_or_b32_e32 v34, 1, v95
	v_cmp_gt_u32_e64 s[0:1], 9, v34
	s_and_b64 s[18:19], s[0:1], s[2:3]
	s_and_saveexec_b64 s[0:1], s[18:19]
	v_add_u32_e32 v34, v34, v42
	v_mul_f32_e32 v35, 0x3e000000, v35
	v_mad_u32_u24 v34, v34, 48, v38
	ds_write_b32 v34, v35 offset:34816
	s_or_b64 exec, exec, s[0:1]
	v_or_b32_e32 v34, 2, v95
	v_cmp_gt_u32_e64 s[0:1], 9, v34
	s_and_b64 s[18:19], s[0:1], s[2:3]
	s_and_saveexec_b64 s[0:1], s[18:19]
	v_add_u32_e32 v34, v34, v42
	v_mul_f32_e32 v35, 0x3e000000, v36
	v_mad_u32_u24 v34, v34, 48, v38
	ds_write_b32 v34, v35 offset:34816
	s_or_b64 exec, exec, s[0:1]
	v_or_b32_e32 v34, 3, v95
	v_cmp_gt_u32_e64 s[0:1], 9, v34
	s_and_b64 s[0:1], s[0:1], s[2:3]
	s_and_b64 exec, exec, s[0:1]
	v_add_u32_e32 v34, v34, v42
	v_mul_f32_e32 v35, 0x3e000000, v37
	v_mad_u32_u24 v34, v34, 48, v38
	ds_write_b32 v34, v35 offset:34816
.LBB1_27:
	s_or_b64 exec, exec, s[4:5]
	s_movk_i32 s0, 0x80
	v_cmp_gt_u32_e64 s[0:1], s0, v0
	s_and_saveexec_b64 s[4:5], s[0:1]
	s_cbranch_execz .LBB1_36
	v_or_b32_e32 v1, 12, v1
	v_add_u32_e32 v34, v1, v39
	s_movk_i32 s0, 0x110
	v_mad_u32_u24 v39, v34, s0, v40
	ds_read_b128 v[34:37], v39
	ds_read_b128 v[42:45], v39 offset:64
	ds_read_b128 v[46:49], v39 offset:128
	ds_read_b128 v[50:53], v39 offset:192
	v_cmp_ne_u32_e64 s[0:1], 3, v90
	v_mul_u32_u24_e32 v39, 9, v1
	s_waitcnt lgkmcnt(0)
	v_mfma_f32_16x16x32_f16 v[34:37], v[34:37], v[46:49], 0
	s_and_b64 s[18:19], s[0:1], s[2:3]
	v_mfma_f32_16x16x32_f16 v[34:37], v[42:45], v[50:53], v[34:37]
	s_and_saveexec_b64 s[0:1], s[18:19]
	s_nop 6
	v_mul_f32_e32 v1, 0x3e000000, v34
	v_add_u32_e32 v34, v95, v39
	v_mad_u32_u24 v34, v34, 48, v38
	ds_write_b32 v34, v1 offset:34816
	s_or_b64 exec, exec, s[0:1]
	v_or_b32_e32 v34, 1, v95
	v_cmp_gt_u32_e64 s[0:1], 9, v34
	s_and_b64 s[18:19], s[0:1], s[2:3]
	s_and_saveexec_b64 s[0:1], s[18:19]
	v_add_u32_e32 v34, v34, v39
	v_mul_f32_e32 v1, 0x3e000000, v35
	v_mad_u32_u24 v34, v34, 48, v38
	ds_write_b32 v34, v1 offset:34816
	s_or_b64 exec, exec, s[0:1]
	v_or_b32_e32 v34, 2, v95
	v_cmp_gt_u32_e64 s[0:1], 9, v34
	s_and_b64 s[18:19], s[0:1], s[2:3]
	s_and_saveexec_b64 s[0:1], s[18:19]
	v_add_u32_e32 v34, v34, v39
	v_mul_f32_e32 v1, 0x3e000000, v36
	v_mad_u32_u24 v34, v34, 48, v38
	ds_write_b32 v34, v1 offset:34816
	s_or_b64 exec, exec, s[0:1]
	v_or_b32_e32 v34, 3, v95
	v_cmp_gt_u32_e64 s[0:1], 9, v34
	s_and_b64 s[0:1], s[0:1], s[2:3]
	s_and_b64 exec, exec, s[0:1]
	v_add_u32_e32 v34, v34, v39
	v_mul_f32_e32 v1, 0x3e000000, v37
	v_mad_u32_u24 v34, v34, 48, v38
	ds_write_b32 v34, v1 offset:34816
.LBB1_36:
	s_or_b64 exec, exec, s[4:5]
	v_add_u32_e32 v46, v41, v94
	v_mad_u64_u32 v[34:35], s[0:1], v46, 9, v[100:101]
	v_mul_lo_u32 v1, v34, 48
	s_waitcnt lgkmcnt(0)
	s_barrier
	ds_read_b128 v[36:39], v1 offset:34816
	ds_read_b128 v[40:43], v1 offset:34832
	ds_read_b32 v1, v1 offset:34848
	v_and_b32_e32 v47, 1, v0
	v_cmp_lt_u32_e64 s[2:3], 13, v94
	s_waitcnt lgkmcnt(2)
	v_max3_f32 v34, v36, v37, v38
	s_waitcnt lgkmcnt(1)
	v_max3_f32 v34, v34, v39, v40
	v_max3_f32 v34, v34, v41, v42
	s_waitcnt lgkmcnt(0)
	v_max3_f32 v34, v34, v43, v1
	v_sub_f32_e32 v35, v36, v34
	v_mul_f32_e32 v35, 0x3fb8aa3b, v35
	v_sub_f32_e32 v36, v37, v34
	v_exp_f32_e32 v35, v35
	v_mul_f32_e32 v36, 0x3fb8aa3b, v36
	v_sub_f32_e32 v37, v38, v34
	v_exp_f32_e32 v36, v36
	v_mul_f32_e32 v37, 0x3fb8aa3b, v37
	v_sub_f32_e32 v38, v39, v34
	v_exp_f32_e32 v37, v37
	v_mul_f32_e32 v38, 0x3fb8aa3b, v38
	v_sub_f32_e32 v39, v40, v34
	v_exp_f32_e32 v38, v38
	v_mul_f32_e32 v39, 0x3fb8aa3b, v39
	v_add_f32_e32 v44, 0, v35
	v_exp_f32_e32 v39, v39
	v_add_f32_e32 v40, v44, v36
	v_add_f32_e32 v40, v40, v37
	v_add_f32_e32 v40, v40, v38
	v_add_f32_e32 v44, v40, v39
	v_sub_f32_e32 v40, v41, v34
	v_mul_f32_e32 v40, 0x3fb8aa3b, v40
	v_sub_f32_e32 v41, v42, v34
	v_exp_f32_e32 v40, v40
	v_mul_f32_e32 v41, 0x3fb8aa3b, v41
	v_sub_f32_e32 v42, v43, v34
	v_exp_f32_e32 v41, v41
	v_mul_f32_e32 v42, 0x3fb8aa3b, v42
	v_sub_f32_e32 v1, v1, v34
	v_exp_f32_e32 v42, v42
	v_mul_f32_e32 v1, 0x3fb8aa3b, v1
	v_exp_f32_e32 v43, v1
	v_add_f32_e32 v1, v44, v40
	v_add_f32_e32 v1, v1, v41
	v_add_f32_e32 v1, v1, v42
	v_add_f32_e32 v1, v1, v43
	v_rcp_f32_e32 v44, v1
	s_and_b64 s[4:5], vcc, s[2:3]
	v_cmp_eq_u32_e64 s[0:1], 0, v47
	s_and_b64 s[4:5], s[0:1], s[4:5]
	s_xor_b64 s[4:5], s[4:5], -1
	v_lshlrev_b32_e32 v34, 5, v46
	s_and_saveexec_b64 s[18:19], s[4:5]
	s_xor_b64 s[4:5], exec, s[18:19]
	v_lshlrev_b32_e32 v34, 5, v46
	s_or_saveexec_b64 s[4:5], s[4:5]
	v_mul_f32_e32 v55, v44, v35
	v_mul_f32_e32 v54, v44, v36
	v_mul_f32_e32 v53, v44, v37
	v_mul_f32_e32 v52, v44, v38
	v_mul_f32_e32 v51, v44, v39
	v_mul_f32_e32 v50, v44, v40
	v_mul_f32_e32 v49, v44, v41
	v_mul_f32_e32 v35, v44, v42
	v_mul_f32_e32 v48, v44, v43
	s_xor_b64 exec, exec, s[4:5]
	s_cbranch_execz .LBB1_40
	v_add_f32_e32 v1, 0, v55
	v_add_f32_e32 v1, v1, v54
	v_add_f32_e32 v1, v1, v53
	v_add_f32_e32 v1, v1, v52
	v_add_f32_e32 v1, v1, v51
	v_add_f32_e32 v1, v1, v50
	v_add_f32_e32 v1, v1, v49
	v_add_f32_e32 v1, v1, v35
	v_add_f32_e32 v1, v1, v48
	v_fmamk_f32 v36, v1, 0xbde38e39, v48
	v_fmamk_f32 v37, v1, 0xbde38e39, v35
	v_fmamk_f32 v38, v1, 0xbde38e39, v49
	v_fmamk_f32 v39, v1, 0xbde38e39, v50
	v_fmamk_f32 v40, v1, 0xbde38e39, v51
	v_fmamk_f32 v41, v1, 0xbde38e39, v52
	v_fmamk_f32 v42, v1, 0xbde38e39, v53
	v_fmamk_f32 v43, v1, 0xbde38e39, v54
	v_fmamk_f32 v1, v1, 0xbde38e39, v55
	v_fma_f32 v1, v1, v1, 0
	v_fmac_f32_e32 v1, v43, v43
	v_fmac_f32_e32 v1, v42, v42
	v_fmac_f32_e32 v1, v41, v41
	v_fmac_f32_e32 v1, v40, v40
	v_fmac_f32_e32 v1, v39, v39
	v_fmac_f32_e32 v1, v38, v38
	v_fmac_f32_e32 v1, v37, v37
	v_fmac_f32_e32 v1, v36, v36
	v_lshl_add_u32 v36, v100, 2, v34
	ds_write_b32 v36, v1 offset:34268
.LBB1_40:
	s_or_b64 exec, exec, s[4:5]
	s_waitcnt lgkmcnt(0)
	s_barrier
	ds_read_b128 v[56:59], v34 offset:34272
	ds_read_b128 v[60:63], v34 offset:34288
	v_add_u32_e32 v36, s16, v46
	s_movk_i32 s4, 0x628
	v_cmp_gt_i32_e64 s[4:5], s4, v36
	s_and_b64 s[4:5], vcc, s[4:5]
	s_waitcnt lgkmcnt(1)
	v_cmp_gt_f32_e32 vcc, v57, v56
	s_nop 1
	v_cndmask_b32_e64 v1, 0, 1, vcc
	v_cmp_gt_f32_e32 vcc, v58, v56
	s_nop 1
	v_cndmask_b32_e64 v34, 0, 1, vcc
	v_cmp_gt_f32_e32 vcc, v59, v56
	s_nop 1
	v_addc_co_u32_e32 v1, vcc, v1, v34, vcc
	s_waitcnt lgkmcnt(0)
	v_cmp_gt_f32_e32 vcc, v60, v56
	s_nop 1
	v_cndmask_b32_e64 v34, 0, 1, vcc
	v_cmp_gt_f32_e32 vcc, v61, v56
	s_nop 1
	v_addc_co_u32_e32 v1, vcc, v1, v34, vcc
	v_cmp_gt_f32_e32 vcc, v62, v56
	s_nop 1
	v_cndmask_b32_e64 v34, 0, 1, vcc
	v_cmp_gt_f32_e32 vcc, v63, v56
	s_nop 1
	v_addc_co_u32_e32 v34, vcc, v1, v34, vcc
	v_cmp_eq_u32_e32 vcc, 5, v34
	s_nop 1
	v_cndmask_b32_e32 v1, 0, v56, vcc
	v_cmp_eq_u32_e32 vcc, 6, v34
	s_nop 1
	v_cndmask_b32_e32 v38, 0, v56, vcc
	v_cmp_ge_f32_e32 vcc, v56, v57
	s_nop 1
	v_cndmask_b32_e64 v37, 0, 1, vcc
	v_cmp_gt_f32_e32 vcc, v58, v57
	s_nop 1
	v_cndmask_b32_e64 v39, 0, 1, vcc
	v_cmp_gt_f32_e32 vcc, v59, v57
	s_nop 1
	v_addc_co_u32_e32 v37, vcc, v37, v39, vcc
	v_cmp_gt_f32_e32 vcc, v60, v57
	s_nop 1
	v_cndmask_b32_e64 v39, 0, 1, vcc
	v_cmp_gt_f32_e32 vcc, v61, v57
	s_nop 1
	v_addc_co_u32_e32 v37, vcc, v37, v39, vcc
	v_cmp_gt_f32_e32 vcc, v62, v57
	s_nop 1
	v_cndmask_b32_e64 v39, 0, 1, vcc
	v_cmp_gt_f32_e32 vcc, v63, v57
	s_nop 1
	v_addc_co_u32_e32 v37, vcc, v37, v39, vcc
	v_cmp_eq_u32_e32 vcc, 5, v37
	s_nop 1
	v_cndmask_b32_e32 v1, v1, v57, vcc
	v_cmp_eq_u32_e32 vcc, 6, v37
	s_nop 1
	v_cndmask_b32_e32 v39, v38, v57, vcc
	v_cmp_ge_f32_e32 vcc, v56, v58
	s_nop 1
	v_cndmask_b32_e64 v38, 0, 1, vcc
	v_cmp_ge_f32_e32 vcc, v57, v58
	s_nop 1
	v_cndmask_b32_e64 v40, 0, 1, vcc
	v_cmp_gt_f32_e32 vcc, v59, v58
	s_nop 1
	v_addc_co_u32_e32 v38, vcc, v38, v40, vcc
	v_cmp_gt_f32_e32 vcc, v60, v58
	s_nop 1
	v_cndmask_b32_e64 v40, 0, 1, vcc
	v_cmp_gt_f32_e32 vcc, v61, v58
	s_nop 1
	v_addc_co_u32_e32 v38, vcc, v38, v40, vcc
	v_cmp_gt_f32_e32 vcc, v62, v58
	s_nop 1
	v_cndmask_b32_e64 v40, 0, 1, vcc
	v_cmp_gt_f32_e32 vcc, v63, v58
	s_nop 1
	v_addc_co_u32_e32 v38, vcc, v38, v40, vcc
	v_cmp_eq_u32_e32 vcc, 5, v38
	s_nop 1
	v_cndmask_b32_e32 v1, v1, v58, vcc
	v_cmp_eq_u32_e32 vcc, 6, v38
	s_nop 1
	v_cndmask_b32_e32 v40, v39, v58, vcc
	v_cmp_ge_f32_e32 vcc, v56, v59
	s_nop 1
	v_cndmask_b32_e64 v39, 0, 1, vcc
	v_cmp_ge_f32_e32 vcc, v57, v59
	s_nop 1
	v_cndmask_b32_e64 v41, 0, 1, vcc
	v_cmp_ge_f32_e32 vcc, v58, v59
	s_nop 1
	v_addc_co_u32_e32 v39, vcc, v39, v41, vcc
	v_cmp_gt_f32_e32 vcc, v60, v59
	s_nop 1
	v_cndmask_b32_e64 v41, 0, 1, vcc
	v_cmp_gt_f32_e32 vcc, v61, v59
	s_nop 1
	v_addc_co_u32_e32 v39, vcc, v39, v41, vcc
	v_cmp_gt_f32_e32 vcc, v62, v59
	s_nop 1
	v_cndmask_b32_e64 v41, 0, 1, vcc
	v_cmp_gt_f32_e32 vcc, v63, v59
	s_nop 1
	v_addc_co_u32_e32 v39, vcc, v39, v41, vcc
	v_cmp_eq_u32_e32 vcc, 5, v39
	s_nop 1
	v_cndmask_b32_e32 v1, v1, v59, vcc
	v_cmp_eq_u32_e32 vcc, 6, v39
	s_nop 1
	v_cndmask_b32_e32 v41, v40, v59, vcc
	v_cmp_ge_f32_e32 vcc, v56, v60
	s_nop 1
	v_cndmask_b32_e64 v40, 0, 1, vcc
	v_cmp_ge_f32_e32 vcc, v57, v60
	s_nop 1
	v_cndmask_b32_e64 v42, 0, 1, vcc
	v_cmp_ge_f32_e32 vcc, v58, v60
	s_nop 1
	v_addc_co_u32_e32 v40, vcc, v40, v42, vcc
	v_cmp_ge_f32_e32 vcc, v59, v60
	s_nop 1
	v_cndmask_b32_e64 v42, 0, 1, vcc
	v_cmp_gt_f32_e32 vcc, v61, v60
	s_nop 1
	v_addc_co_u32_e32 v40, vcc, v40, v42, vcc
	v_cmp_gt_f32_e32 vcc, v62, v60
	s_nop 1
	v_cndmask_b32_e64 v42, 0, 1, vcc
	v_cmp_gt_f32_e32 vcc, v63, v60
	s_nop 1
	v_addc_co_u32_e32 v40, vcc, v40, v42, vcc
	v_cmp_eq_u32_e32 vcc, 5, v40
	s_nop 1
	v_cndmask_b32_e32 v1, v1, v60, vcc
	v_cmp_eq_u32_e32 vcc, 6, v40
	s_nop 1
	v_cndmask_b32_e32 v42, v41, v60, vcc
	v_cmp_ge_f32_e32 vcc, v56, v61
	s_nop 1
	v_cndmask_b32_e64 v41, 0, 1, vcc
	v_cmp_ge_f32_e32 vcc, v57, v61
	s_nop 1
	v_cndmask_b32_e64 v43, 0, 1, vcc
	v_cmp_ge_f32_e32 vcc, v58, v61
	s_nop 1
	v_addc_co_u32_e32 v41, vcc, v41, v43, vcc
	v_cmp_ge_f32_e32 vcc, v59, v61
	s_nop 1
	v_cndmask_b32_e64 v43, 0, 1, vcc
	v_cmp_ge_f32_e32 vcc, v60, v61
	s_nop 1
	v_addc_co_u32_e32 v41, vcc, v41, v43, vcc
	v_cmp_gt_f32_e32 vcc, v62, v61
	s_nop 1
	v_cndmask_b32_e64 v43, 0, 1, vcc
	v_cmp_gt_f32_e32 vcc, v63, v61
	s_nop 1
	v_addc_co_u32_e32 v41, vcc, v41, v43, vcc
	v_cmp_eq_u32_e32 vcc, 5, v41
	s_nop 1
	v_cndmask_b32_e32 v1, v1, v61, vcc
	v_cmp_eq_u32_e32 vcc, 6, v41
	s_nop 1
	v_cndmask_b32_e32 v43, v42, v61, vcc
	v_cmp_ge_f32_e32 vcc, v56, v62
	s_nop 1
	v_cndmask_b32_e64 v42, 0, 1, vcc
	v_cmp_ge_f32_e32 vcc, v57, v62
	s_nop 1
	v_cndmask_b32_e64 v44, 0, 1, vcc
	v_cmp_ge_f32_e32 vcc, v58, v62
	s_nop 1
	v_addc_co_u32_e32 v42, vcc, v42, v44, vcc
	v_cmp_ge_f32_e32 vcc, v59, v62
	s_nop 1
	v_cndmask_b32_e64 v44, 0, 1, vcc
	v_cmp_ge_f32_e32 vcc, v60, v62
	s_nop 1
	v_addc_co_u32_e32 v42, vcc, v42, v44, vcc
	v_cmp_ge_f32_e32 vcc, v61, v62
	s_nop 1
	v_cndmask_b32_e64 v44, 0, 1, vcc
	v_cmp_gt_f32_e32 vcc, v63, v62
	s_nop 1
	v_addc_co_u32_e32 v42, vcc, v42, v44, vcc
	v_cmp_eq_u32_e32 vcc, 5, v42
	s_nop 1
	v_cndmask_b32_e32 v1, v1, v62, vcc
	v_cmp_eq_u32_e32 vcc, 6, v42
	s_nop 1
	v_cndmask_b32_e32 v44, v43, v62, vcc
	v_cmp_ge_f32_e32 vcc, v56, v63
	s_nop 1
	v_cndmask_b32_e64 v43, 0, 1, vcc
	v_cmp_ge_f32_e32 vcc, v57, v63
	s_nop 1
	v_cndmask_b32_e64 v45, 0, 1, vcc
	v_cmp_ge_f32_e32 vcc, v58, v63
	s_nop 1
	v_addc_co_u32_e32 v43, vcc, v43, v45, vcc
	v_cmp_ge_f32_e32 vcc, v59, v63
	s_nop 1
	v_cndmask_b32_e64 v45, 0, 1, vcc
	v_cmp_ge_f32_e32 vcc, v60, v63
	s_nop 1
	v_addc_co_u32_e32 v43, vcc, v43, v45, vcc
	v_cmp_ge_f32_e32 vcc, v61, v63
	s_nop 1
	v_cndmask_b32_e64 v45, 0, 1, vcc
	v_cmp_ge_f32_e32 vcc, v62, v63
	s_nop 1
	v_addc_co_u32_e32 v43, vcc, v43, v45, vcc
	v_cmp_eq_u32_e32 vcc, 5, v43
	v_add_u32_e32 v45, -14, v94
	s_nop 0
	v_cndmask_b32_e32 v1, v1, v63, vcc
	v_cmp_eq_u32_e32 vcc, 6, v43
	v_mul_f32_e32 v1, 0x3f7eb8bb, v1
	s_nop 0
	v_cndmask_b32_e32 v44, v44, v63, vcc
	v_cmp_gt_u32_e32 vcc, 14, v45
	s_and_b64 s[16:17], s[4:5], vcc
	s_and_b64 s[16:17], s[0:1], s[16:17]
	v_cmp_nle_f32_e32 vcc, v44, v1
	s_and_b64 s[18:19], s[16:17], vcc
	s_and_saveexec_b64 s[16:17], s[18:19]
	s_cbranch_execz .LBB1_44
	s_mov_b64 s[20:21], exec
	v_mbcnt_lo_u32_b32 v1, s20, 0
	v_mbcnt_hi_u32_b32 v44, s21, v1
	v_cmp_eq_u32_e32 vcc, 0, v44
	s_and_saveexec_b64 s[18:19], vcc
	s_cbranch_execz .LBB1_43
	s_bcnt1_i32_b64 s20, s[20:21]
	v_mov_b32_e32 v1, 0
	v_mov_b32_e32 v45, s20
	global_atomic_add v45, v1, v45, s[10:11] sc0

.LBB1_46:
	s_or_b64 exec, exec, s[10:11]
	s_lshl_b32 s10, s22, 3
	v_ashrrev_i32_e32 v34, 3, v36
	v_and_or_b32 v36, v36, 7, s10
	v_mad_u32_u24 v56, v36, 7, v45
	s_and_saveexec_b64 s[10:11], s[0:1]
	s_movk_i32 s16, 0xc5
	v_mad_u32_u24 v1, v56, s16, v34
	v_cndmask_b32_e64 v1, -1, v1, s[4:5]
	v_lshlrev_b32_e32 v37, 2, v93
	ds_write_b32 v37, v1 offset:34816
	s_or_b64 exec, exec, s[10:11]
	s_and_b64 s[10:11], s[4:5], s[2:3]
	s_and_saveexec_b64 s[2:3], s[10:11]
	s_cbranch_execz .LBB1_52
	s_movk_i32 s10, 0xc5
	v_mad_u32_u24 v1, v36, s10, v34
	s_movk_i32 s10, 0xd8
	v_mov_b64_e32 v[36:37], s[8:9]
	v_cvt_f32_u32_e32 v57, v44
	v_mad_i64_i32 v[36:37], s[8:9], v1, s10, v[36:37]
	v_mul_i32_i24_e32 v1, 9, v45
	v_lshlrev_b32_e32 v38, 2, v1
	v_mov_b32_e32 v39, 0
	v_lshl_add_u64 v[36:37], v[36:37], 0, v[38:39]
	v_mov_b64_e32 v[38:39], -4
	v_mov_b64_e32 v[40:41], -8
	v_mov_b64_e32 v[42:43], -12
	v_mov_b64_e32 v[44:45], -16
	s_and_saveexec_b64 s[8:9], s[0:1]
	s_cbranch_execz .LBB1_51
	v_not_b32_e32 v38, 19
	v_not_b32_e32 v40, 23
	v_not_b32_e32 v42, 27
	v_not_b32_e32 v44, 31
	v_mov_b32_e32 v39, -1
	v_mov_b32_e32 v41, -1
	v_mov_b32_e32 v43, -1
	v_mov_b32_e32 v45, -1
	global_store_dword v[36:37], v57, off offset:-36

.LBB1_52:
	s_or_b64 exec, exec, s[2:3]
	v_lshlrev_b32_e32 v43, 2, v64
	s_waitcnt lgkmcnt(0)
	s_barrier
	ds_read_b32 v42, v43 offset:34816
	v_lshlrev_b32_e32 v1, 3, v0
	v_and_b32_e32 v1, 56, v1
	v_lshlrev_b32_e32 v40, 1, v1
	v_mov_b32_e32 v41, 0
	v_lshl_add_u64 v[38:39], s[12:13], 0, v[40:41]
	v_lshl_add_u64 v[36:37], s[14:15], 0, v[40:41]
	s_waitcnt lgkmcnt(0)
	v_cmp_lt_i32_e32 vcc, -1, v42
	s_and_saveexec_b64 s[0:1], vcc
	s_cbranch_execz .LBB1_54
	v_mul_u32_u24_e32 v1, 0x10c, v64
	v_add3_u32 v1, v43, v1, v40
	ds_read_b128 v[58:61], v1
	ds_read_b128 v[62:65], v1 offset:128
	v_mov_b32_e32 v43, v41
	v_lshlrev_b64 v[42:43], 7, v[42:43]
	v_lshl_add_u64 v[44:45], v[38:39], 0, v[42:43]
	v_lshl_add_u64 v[42:43], v[36:37], 0, v[42:43]
	s_waitcnt lgkmcnt(1)
	global_store_dwordx4 v[44:45], v[58:61], off
	s_waitcnt lgkmcnt(0)
	global_store_dwordx4 v[42:43], v[62:65], off
.LBB1_54:
	s_or_b64 exec, exec, s[0:1]
	v_or_b32_e32 v1, 0x100, v0
	v_lshrrev_b32_e32 v1, 3, v1
	v_lshlrev_b32_e32 v41, 2, v1
	ds_read_b32 v42, v41 offset:34816
	s_waitcnt lgkmcnt(0)
	v_cmp_lt_i32_e32 vcc, -1, v42
	s_and_saveexec_b64 s[0:1], vcc
	s_cbranch_execz .LBB1_56
	v_mul_u32_u24_e32 v1, 0x10c, v1
	v_add3_u32 v1, v41, v1, v40
	ds_read_b128 v[58:61], v1
	ds_read_b128 v[62:65], v1 offset:128
	v_mov_b32_e32 v43, 0
	v_lshlrev_b64 v[42:43], 7, v[42:43]
	v_lshl_add_u64 v[44:45], v[38:39], 0, v[42:43]
	v_lshl_add_u64 v[42:43], v[36:37], 0, v[42:43]
	s_waitcnt lgkmcnt(1)
	global_store_dwordx4 v[44:45], v[58:61], off
	s_waitcnt lgkmcnt(0)
	global_store_dwordx4 v[42:43], v[62:65], off
.LBB1_56:
	s_or_b64 exec, exec, s[0:1]
	v_or_b32_e32 v1, 0x200, v0
	v_lshrrev_b32_e32 v1, 3, v1
	v_lshlrev_b32_e32 v41, 2, v1
	ds_read_b32 v42, v41 offset:34816
	s_waitcnt lgkmcnt(0)
	v_cmp_lt_i32_e32 vcc, -1, v42
	s_and_saveexec_b64 s[0:1], vcc
	s_cbranch_execz .LBB1_58
	v_mul_u32_u24_e32 v1, 0x10c, v1
	v_add3_u32 v1, v41, v1, v40
	ds_read_b128 v[58:61], v1
	ds_read_b128 v[62:65], v1 offset:128
	v_mov_b32_e32 v43, 0
	v_lshlrev_b64 v[42:43], 7, v[42:43]
	v_lshl_add_u64 v[44:45], v[38:39], 0, v[42:43]
	v_lshl_add_u64 v[42:43], v[36:37], 0, v[42:43]
	s_waitcnt lgkmcnt(1)
	global_store_dwordx4 v[44:45], v[58:61], off
	s_waitcnt lgkmcnt(0)
	global_store_dwordx4 v[42:43], v[62:65], off
.LBB1_58:
	s_or_b64 exec, exec, s[0:1]
	v_or_b32_e32 v0, 0x300, v0
	v_lshrrev_b32_e32 v1, 3, v0
	v_lshlrev_b32_e32 v41, 2, v1
	ds_read_b32 v0, v41 offset:34816
	s_waitcnt lgkmcnt(0)
	v_cmp_lt_i32_e32 vcc, -1, v0
	s_and_saveexec_b64 s[0:1], vcc
	s_cbranch_execz .LBB1_60
	v_mul_u32_u24_e32 v1, 0x10c, v1
	v_add3_u32 v44, v41, v1, v40
	ds_read_b128 v[40:43], v44
	ds_read_b128 v[58:61], v44 offset:128
	v_mov_b32_e32 v1, 0
	v_lshlrev_b64 v[0:1], 7, v[0:1]
	v_lshl_add_u64 v[38:39], v[38:39], 0, v[0:1]
	v_lshl_add_u64 v[0:1], v[36:37], 0, v[0:1]
	s_waitcnt lgkmcnt(1)
	global_store_dwordx4 v[38:39], v[40:43], off
	s_waitcnt lgkmcnt(0)
	global_store_dwordx4 v[0:1], v[58:61], off

	.amdhsa_kernel _Z14k_qkv_temporalPKDF16_S0_PKfPDF16_S3_S3_PfPi
		.amdhsa_group_segment_fixed_size 40960
		.amdhsa_private_segment_fixed_size 0
		.amdhsa_kernarg_size 64
		.amdhsa_user_sgpr_count 2
		.amdhsa_user_sgpr_dispatch_ptr 0
		.amdhsa_user_sgpr_queue_ptr 0
		.amdhsa_user_sgpr_kernarg_segment_ptr 1
		.amdhsa_user_sgpr_dispatch_id 0
		.amdhsa_user_sgpr_kernarg_preload_length 0
		.amdhsa_user_sgpr_kernarg_preload_offset 0
		.amdhsa_user_sgpr_private_segment_size 0
		.amdhsa_uses_dynamic_stack 0
		.amdhsa_enable_private_segment 0
		.amdhsa_system_sgpr_workgroup_id_x 1
		.amdhsa_system_sgpr_workgroup_id_y 0
		.amdhsa_system_sgpr_workgroup_id_z 0
		.amdhsa_system_sgpr_workgroup_info 0
		.amdhsa_system_vgpr_workitem_id 0
		.amdhsa_next_free_vgpr 128
		.amdhsa_next_free_sgpr 96
		.amdhsa_accum_offset 128
		.amdhsa_reserve_vcc 1
		.amdhsa_float_round_mode_32 0
		.amdhsa_float_round_mode_16_64 0
		.amdhsa_float_denorm_mode_32 3
		.amdhsa_float_denorm_mode_16_64 3
		.amdhsa_dx10_clamp 1
		.amdhsa_ieee_mode 1
		.amdhsa_fp16_overflow 0
		.amdhsa_tg_split 0
		.amdhsa_exception_fp_ieee_invalid_op 0
		.amdhsa_exception_fp_denorm_src 0
		.amdhsa_exception_fp_ieee_div_zero 0
		.amdhsa_exception_fp_ieee_overflow 0
		.amdhsa_exception_fp_ieee_underflow 0
		.amdhsa_exception_fp_ieee_inexact 0
		.amdhsa_exception_int_div_zero 0
	.end_amdhsa_kernel

amdhsa.kernels:
  - .agpr_count:     0
    .args:
      - .actual_access:  read_only
        .address_space:  global
        .offset:         0
        .size:           8
        .value_kind:     global_buffer
      - .actual_access:  read_only
        .address_space:  global
        .offset:         8
        .size:           8
        .value_kind:     global_buffer
      - .actual_access:  read_only
        .address_space:  global
        .offset:         16
        .size:           8
        .value_kind:     global_buffer
      - .actual_access:  write_only
        .address_space:  global
        .offset:         24
        .size:           8
        .value_kind:     global_buffer
      - .actual_access:  write_only
        .address_space:  global
        .offset:         32
        .size:           8
        .value_kind:     global_buffer
      - .actual_access:  write_only
        .address_space:  global
        .offset:         40
        .size:           8
        .value_kind:     global_buffer
      - .actual_access:  write_only
        .address_space:  global
        .offset:         48
        .size:           8
        .value_kind:     global_buffer
    .group_segment_fixed_size: 0
    .kernarg_segment_align: 8
    .kernarg_segment_size: 56
    .language:       OpenCL C
    .language_version:
      - 2
      - 0
    .max_flat_workgroup_size: 256
    .name:           _Z6k_prepPKfS0_S0_PDF16_S1_S1_Pi
    .private_segment_fixed_size: 0
    .sgpr_count:     16
    .sgpr_spill_count: 0
    .symbol:         _Z6k_prepPKfS0_S0_PDF16_S1_S1_Pi.kd
    .uniform_work_group_size: 1
    .uses_dynamic_stack: false
    .vgpr_count:     14
    .vgpr_spill_count: 0
    .wavefront_size: 64
  - .agpr_count:     0
    .args:
      - .address_space:  global
        .offset:         0
        .size:           8
        .value_kind:     global_buffer
      - .address_space:  global
        .offset:         8
        .size:           8
        .value_kind:     global_buffer
      - .actual_access:  read_only
        .address_space:  global
        .offset:         16
        .size:           8
        .value_kind:     global_buffer
      - .actual_access:  write_only
        .address_space:  global
        .offset:         24
        .size:           8
        .value_kind:     global_buffer
      - .actual_access:  write_only
        .address_space:  global
        .offset:         32
        .size:           8
        .value_kind:     global_buffer
      - .actual_access:  write_only
        .address_space:  global
        .offset:         40
        .size:           8
        .value_kind:     global_buffer
      - .actual_access:  write_only
        .address_space:  global
        .offset:         48
        .size:           8
        .value_kind:     global_buffer
      - .address_space:  global
        .offset:         56
        .size:           8
        .value_kind:     global_buffer
    .group_segment_fixed_size: 40960
    .kernarg_segment_align: 8
    .kernarg_segment_size: 64
    .language:       OpenCL C
    .language_version:
      - 2
      - 0
    .max_flat_workgroup_size: 256
    .name:           _Z14k_qkv_temporalPKDF16_S0_PKfPDF16_S3_S3_PfPi
    .private_segment_fixed_size: 0
    .sgpr_count:     29
    .sgpr_spill_count: 0
    .symbol:         _Z14k_qkv_temporalPKDF16_S0_PKfPDF16_S3_S3_PfPi.kd
    .uniform_work_group_size: 1
    .uses_dynamic_stack: false
    .vgpr_count:     128
    .vgpr_spill_count: 0
    .wavefront_size: 64
  - .agpr_count:     8
    .args:
      - .actual_access:  read_only
        .address_space:  global
        .offset:         0
        .size:           8
        .value_kind:     global_buffer
      - .actual_access:  read_only
        .address_space:  global
        .offset:         8
        .size:           8
        .value_kind:     global_buffer
      - .actual_access:  read_only
        .address_space:  global
        .offset:         16
        .size:           8
        .value_kind:     global_buffer
      - .actual_access:  write_only
        .address_space:  global
        .offset:         24
        .size:           8
        .value_kind:     global_buffer
      - .actual_access:  write_only
        .address_space:  global
        .offset:         32
        .size:           8
        .value_kind:     global_buffer
      - .actual_access:  write_only
        .address_space:  global
        .offset:         40
        .size:           8
        .value_kind:     global_buffer
      - .address_space:  global
        .offset:         48
        .size:           8
        .value_kind:     global_buffer
      - .actual_access:  read_only
        .address_space:  global
        .offset:         56
        .size:           8
        .value_kind:     global_buffer
      - .offset:         64
        .size:           4
        .value_kind:     hidden_block_count_x
      - .offset:         68
        .size:           4
        .value_kind:     hidden_block_count_y
      - .offset:         72
        .size:           4
        .value_kind:     hidden_block_count_z
      - .offset:         76
        .size:           2
        .value_kind:     hidden_group_size_x
      - .offset:         78
        .size:           2
        .value_kind:     hidden_group_size_y
      - .offset:         80
        .size:           2
        .value_kind:     hidden_group_size_z
      - .offset:         82
        .size:           2
        .value_kind:     hidden_remainder_x
      - .offset:         84
        .size:           2
        .value_kind:     hidden_remainder_y
      - .offset:         86
        .size:           2
        .value_kind:     hidden_remainder_z
      - .offset:         104
        .size:           8
        .value_kind:     hidden_global_offset_x
      - .offset:         112
        .size:           8
        .value_kind:     hidden_global_offset_y
      - .offset:         120
        .size:           8
        .value_kind:     hidden_global_offset_z
      - .offset:         128
        .size:           2
        .value_kind:     hidden_grid_dims
    .group_segment_fixed_size: 9568
    .kernarg_segment_align: 8
    .kernarg_segment_size: 320
    .language:       OpenCL C
    .language_version:
      - 2
      - 0
    .max_flat_workgroup_size: 256
    .name:           _Z7k_fixupPKfS0_S0_PDF16_S1_S1_PfPKi
    .private_segment_fixed_size: 0
    .sgpr_count:     96
    .sgpr_spill_count: 0
    .symbol:         _Z7k_fixupPKfS0_S0_PDF16_S1_S1_PfPKi.kd
    .uniform_work_group_size: 1
    .uses_dynamic_stack: false
    .vgpr_count:     164
    .vgpr_spill_count: 0
    .wavefront_size: 64
  - .agpr_count:     0
    .args:
      - .actual_access:  read_only
        .address_space:  global
        .offset:         0
        .size:           8
        .value_kind:     global_buffer
      - .actual_access:  read_only
        .address_space:  global
        .offset:         8
        .size:           8
        .value_kind:     global_buffer
      - .actual_access:  read_only
        .address_space:  global
        .offset:         16
        .size:           8
        .value_kind:     global_buffer
      - .actual_access:  write_only
        .address_space:  global
        .offset:         24
        .size:           8
        .value_kind:     global_buffer
      - .actual_access:  write_only
        .address_space:  global
        .offset:         32
        .size:           8
        .value_kind:     global_buffer
    .group_segment_fixed_size: 62336
    .kernarg_segment_align: 8
    .kernarg_segment_size: 40
    .language:       OpenCL C
    .language_version:
      - 2
      - 0
    .max_flat_workgroup_size: 448
    .name:           _Z9k_spatialPKDF16_S0_S0_PfPDF16_
    .private_segment_fixed_size: 0
    .sgpr_count:     19
    .sgpr_spill_count: 0
    .symbol:         _Z9k_spatialPKDF16_S0_S0_PfPDF16_.kd
    .uniform_work_group_size: 1
    .uses_dynamic_stack: false
    .vgpr_count:     128
    .vgpr_spill_count: 0
    .wavefront_size: 64
  - .agpr_count:     0
    .args:
      - .address_space:  global
        .offset:         0
        .size:           8
        .value_kind:     global_buffer
      - .address_space:  global
        .offset:         8
        .size:           8
        .value_kind:     global_buffer
      - .actual_access:  read_only
        .address_space:  global
        .offset:         16
        .size:           8
        .value_kind:     global_buffer
      - .actual_access:  write_only
        .address_space:  global
        .offset:         24
        .size:           8
        .value_kind:     global_buffer
    .group_segment_fixed_size: 65536
    .kernarg_segment_align: 8
    .kernarg_segment_size: 32
    .language:       OpenCL C
    .language_version:
      - 2
      - 0
    .max_flat_workgroup_size: 256
    .name:           _Z9k_outprojPKDF16_S0_PKfPf
    .private_segment_fixed_size: 0
    .sgpr_count:     28
    .sgpr_spill_count: 0
    .symbol:         _Z9k_outprojPKDF16_S0_PKfPf.kd
    .uniform_work_group_size: 1
    .uses_dynamic_stack: false
    .vgpr_count:     107
    .vgpr_spill_count: 0
    .wavefront_size: 64
